# v8 + expert weight conversion loops: vmcnt waits re-derived for the prefetching path (the compiler's counts assumed the conditional next-item loads were not issued), drain only on the last item
# speedup vs baseline: 1.0176x; 1.0176x over previous
.LBB0_219:
	s_add_u32 s7, s82, 0x4000000
	v_readlane_b32 s34, v252, 14
	s_waitcnt lgkmcnt(0)
	s_addc_u32 s10, s83, 0
	s_ashr_i32 s0, s34, 31
	s_lshr_b32 s0, s0, 23
	s_add_i32 s2, s34, s0
	s_ashr_i32 s0, s2, 9
	s_ashr_i32 s1, s0, 31
	s_lshl_b64 s[0:1], s[0:1], 25
	s_add_u32 s0, s16, s0
	s_addc_u32 s1, s17, s1
	s_and_b32 s2, s2, 0xfffffe00
	s_sub_i32 s2, s34, s2
	s_lshr_b32 s3, s2, 3
	s_bfe_i32 s4, s3, 0x80000
	s_bfe_u32 s4, s4, 0x2000d
	s_add_i32 s4, s3, s4
	s_bfe_i32 s5, s4, 0x80000
	s_and_b32 s4, s4, 0xfc
	s_sub_i32 s3, s3, s4
	s_sext_i32_i8 s3, s3
	s_lshl_b32 s2, s2, 6
	s_lshl_b32 s3, s3, 9
	s_and_b32 s4, s2, 0x100
	s_sext_i32_i16 s5, s5
	s_or_b32 s3, s3, s4
	v_and_b32_e32 v137, 48, v0
	s_waitcnt vmcnt(39)
	v_or_b32_e32 v42, s3, v137
	s_lshl_b32 s3, s5, 6
	s_and_b32 s3, s3, 0xffffff00
	s_and_b32 s2, s2, 0xc0
	v_ashrrev_i32_e32 v43, 31, v42
	s_or_b32 s2, s3, s2
	v_lshlrev_b64 v[2:3], 14, v[42:43]
	s_ashr_i32 s3, s2, 31
	v_and_b32_e32 v1, 15, v0
	v_lshl_add_u64 v[2:3], s[0:1], 0, v[2:3]
	s_lshl_b64 s[2:3], s[2:3], 2
	v_mov_b32_e32 v131, 0
	v_lshl_add_u64 v[2:3], v[2:3], 0, s[2:3]
	v_lshlrev_b32_e32 v132, 4, v1
	v_mov_b32_e32 v133, v131
	s_waitcnt vmcnt(35)
	v_lshl_add_u64 v[44:45], v[2:3], 0, v[132:133]
	s_movk_i32 s11, 0x4000
	v_add_co_u32_e32 v10, vcc, s11, v44
	s_mov_b32 s18, 0x8000
	s_nop 0
	v_addc_co_u32_e32 v11, vcc, 0, v45, vcc
	v_add_co_u32_e32 v14, vcc, s18, v44
	s_mov_b32 s19, 0xc000
	s_nop 0
	v_addc_co_u32_e32 v15, vcc, 0, v45, vcc
	v_add_co_u32_e32 v16, vcc, s19, v44
	s_mov_b32 s20, 0x10000
	s_nop 0
	v_addc_co_u32_e32 v17, vcc, 0, v45, vcc
	v_add_co_u32_e32 v26, vcc, s20, v44
	s_mov_b32 s21, 0x14000
	s_nop 0
	v_addc_co_u32_e32 v27, vcc, 0, v45, vcc
	v_add_co_u32_e32 v28, vcc, s21, v44
	s_mov_b32 s22, 0x18000
	s_nop 0
	v_addc_co_u32_e32 v29, vcc, 0, v45, vcc
	v_add_co_u32_e32 v30, vcc, s22, v44
	s_mov_b32 s23, 0x1c000
	s_nop 0
	v_addc_co_u32_e32 v31, vcc, 0, v45, vcc
	v_add_co_u32_e32 v32, vcc, s23, v44
	s_mov_b32 s24, 0x20000
	s_nop 0
	v_addc_co_u32_e32 v33, vcc, 0, v45, vcc
	s_waitcnt vmcnt(34)
	v_add_co_u32_e32 v46, vcc, s24, v44
	s_mov_b32 s25, 0x24000
	s_waitcnt vmcnt(33)
	v_addc_co_u32_e32 v47, vcc, 0, v45, vcc
	s_waitcnt vmcnt(32)
	v_add_co_u32_e32 v48, vcc, s25, v44
	s_mov_b32 s26, 0x28000
	s_waitcnt vmcnt(31)
	v_addc_co_u32_e32 v49, vcc, 0, v45, vcc
	global_load_dwordx4 v[2:5], v[44:45], off nt
	global_load_dwordx4 v[6:9], v[10:11], off nt
	s_nop 0
	global_load_dwordx4 v[10:13], v[14:15], off nt
	global_load_dwordx4 v[18:21], v[16:17], off nt
	s_nop 0
	global_load_dwordx4 v[14:17], v[26:27], off nt
	global_load_dwordx4 v[22:25], v[28:29], off nt
	s_nop 0
	global_load_dwordx4 v[26:29], v[30:31], off nt
	global_load_dwordx4 v[34:37], v[32:33], off nt
	s_nop 0
	global_load_dwordx4 v[30:33], v[46:47], off nt
	global_load_dwordx4 v[38:41], v[48:49], off nt
	v_add_co_u32_e32 v46, vcc, s26, v44
	s_mov_b32 s27, 0x2c000
	s_nop 0
	v_addc_co_u32_e32 v47, vcc, 0, v45, vcc
	v_add_co_u32_e32 v48, vcc, s27, v44
	s_mov_b32 s28, 0x30000
	s_nop 0
	v_addc_co_u32_e32 v49, vcc, 0, v45, vcc
	global_load_dwordx4 v[54:57], v[46:47], off nt
	global_load_dwordx4 v[62:65], v[48:49], off nt
	v_add_co_u32_e32 v46, vcc, s28, v44
	s_mov_b32 s29, 0x34000
	s_nop 0
	v_addc_co_u32_e32 v47, vcc, 0, v45, vcc
	v_add_co_u32_e32 v48, vcc, s29, v44
	v_or_b32_e32 v42, 64, v42
	s_nop 0
	v_addc_co_u32_e32 v49, vcc, 0, v45, vcc
	s_mov_b32 s30, 0x38000
	v_ashrrev_i32_e32 v43, 31, v42
	global_load_dwordx4 v[50:53], v[46:47], off nt
	global_load_dwordx4 v[58:61], v[48:49], off nt
	v_add_co_u32_e32 v46, vcc, s30, v44
	v_lshlrev_b64 v[42:43], 14, v[42:43]
	s_nop 0
	v_addc_co_u32_e32 v47, vcc, 0, v45, vcc
	s_mov_b32 s31, 0x3c000
	v_lshl_add_u64 v[42:43], s[0:1], 0, v[42:43]
	v_add_co_u32_e32 v44, vcc, s31, v44
	v_lshl_add_u64 v[42:43], v[42:43], 0, s[2:3]
	s_nop 0
	v_addc_co_u32_e32 v45, vcc, 0, v45, vcc
	s_waitcnt vmcnt(31)
	v_lshl_add_u64 v[122:123], v[42:43], 0, v[132:133]
	global_load_dwordx4 v[82:85], v[46:47], off nt
	global_load_dwordx4 v[90:93], v[44:45], off nt
	v_add_co_u32_e32 v46, vcc, s11, v122
	s_movk_i32 s0, 0x410
	s_nop 0
	v_addc_co_u32_e32 v47, vcc, 0, v123, vcc
	s_waitcnt vmcnt(30)
	v_add_co_u32_e32 v66, vcc, s18, v122
	global_load_dwordx4 v[42:45], v[122:123], off nt
	s_nop 0
	global_load_dwordx4 v[46:49], v[46:47], off nt
	s_waitcnt vmcnt(31)
	v_addc_co_u32_e32 v67, vcc, 0, v123, vcc
	s_waitcnt vmcnt(30)
	v_add_co_u32_e32 v68, vcc, s19, v122
	v_mov_b32_e32 v141, s6
	s_waitcnt vmcnt(27)
	v_addc_co_u32_e32 v69, vcc, 0, v123, vcc
	global_load_dwordx4 v[70:73], v[66:67], off nt
	global_load_dwordx4 v[78:81], v[68:69], off nt
	v_add_co_u32_e32 v66, vcc, s20, v122
	v_lshlrev_b32_e32 v130, 2, v1
	s_nop 0
	v_addc_co_u32_e32 v67, vcc, 0, v123, vcc
	s_waitcnt vmcnt(24)
	v_add_co_u32_e32 v74, vcc, s21, v122
	v_add_u32_e32 v134, s6, v137
	s_nop 0
	v_addc_co_u32_e32 v75, vcc, 0, v123, vcc
	v_add_co_u32_e32 v86, vcc, s22, v122
	global_load_dwordx4 v[66:69], v[66:67], off nt
	s_nop 0
	global_load_dwordx4 v[74:77], v[74:75], off nt
	v_addc_co_u32_e32 v87, vcc, 0, v123, vcc
	v_add_co_u32_e32 v94, vcc, s23, v122
	v_add_u32_e32 v135, s6, v132
	s_nop 0
	v_addc_co_u32_e32 v95, vcc, 0, v123, vcc
	global_load_dwordx4 v[86:89], v[86:87], off nt
	s_nop 0
	global_load_dwordx4 v[98:101], v[94:95], off nt
	v_add_co_u32_e32 v94, vcc, s24, v122
	v_lshlrev_b32_e32 v139, 3, v198
	s_nop 0
	v_addc_co_u32_e32 v95, vcc, 0, v123, vcc
	v_add_co_u32_e32 v102, vcc, s25, v122
	v_mul_u32_u24_e32 v140, 0x410, v1
	s_nop 0
	v_addc_co_u32_e32 v103, vcc, 0, v123, vcc
	v_add_co_u32_e32 v106, vcc, s26, v122
	global_load_dwordx4 v[94:97], v[94:95], off nt
	s_nop 0
	global_load_dwordx4 v[102:105], v[102:103], off nt
	v_addc_co_u32_e32 v107, vcc, 0, v123, vcc
	v_add_co_u32_e32 v108, vcc, s27, v122
	v_mad_u32_u24 v142, v1, s0, v141
	s_nop 0
	v_addc_co_u32_e32 v109, vcc, 0, v123, vcc
	global_load_dwordx4 v[110:113], v[106:107], off nt
	global_load_dwordx4 v[118:121], v[108:109], off nt
	v_add_co_u32_e32 v106, vcc, s28, v122
	v_mul_u32_u24_e32 v141, 0x104, v136
	s_nop 0
	v_addc_co_u32_e32 v107, vcc, 0, v123, vcc
	v_add_co_u32_e32 v114, vcc, s29, v122
	v_or_b32_e32 v138, 64, v137
	s_nop 0
	v_addc_co_u32_e32 v115, vcc, 0, v123, vcc
	v_add_co_u32_e32 v124, vcc, s30, v122
	global_load_dwordx4 v[106:109], v[106:107], off nt
	s_nop 0
	global_load_dwordx4 v[114:117], v[114:115], off nt
	v_addc_co_u32_e32 v125, vcc, 0, v123, vcc
	v_add_co_u32_e32 v126, vcc, s31, v122
	v_and_b32_e32 v139, 0x80, v139
	s_nop 0
	v_addc_co_u32_e32 v127, vcc, 0, v123, vcc
	global_load_dwordx4 v[122:125], v[124:125], off nt
	s_nop 0
	global_load_dwordx4 v[126:129], v[126:127], off nt
	s_lshl_b32 s35, s34, 6
	s_lshl_b32 s33, s85, 6
	v_add_u32_e32 v140, v134, v140
	v_lshlrev_b32_e32 v130, 2, v130
	v_add_u32_e32 v141, v135, v141
	v_add_u32_e32 v142, v142, v137
	s_waitcnt vmcnt(0)
	s_branch .LBB0_221

.LBB0_221:
	s_waitcnt vmcnt(47)
	v_mul_f32_e32 v134, 0x42800000, v2
	s_waitcnt vmcnt(46)
	v_mul_f32_e32 v6, 0x42800000, v6
	v_mov_b32_e32 v2, v131
	v_cvt_pk_fp8_f32 v2, v134, v6
	v_mul_f32_e32 v3, 0x42800000, v3
	v_mul_f32_e32 v6, 0x42800000, v7
	v_mov_b32_e32 v7, v131
	v_cvt_pk_fp8_f32 v7, v3, v6
	s_waitcnt vmcnt(45)
	v_mul_f32_e32 v3, 0x42800000, v11
	s_waitcnt vmcnt(44)
	v_mul_f32_e32 v6, 0x42800000, v19
	v_mul_f32_e32 v10, 0x42800000, v10
	v_cvt_pk_fp8_f32 v7, v3, v6 op_sel:[0,0,1]
	v_mul_f32_e32 v3, 0x42800000, v4
	v_mul_f32_e32 v4, 0x42800000, v8
	v_mov_b32_e32 v6, v131
	v_cvt_pk_fp8_f32 v6, v3, v4
	v_mul_f32_e32 v18, 0x42800000, v18
	v_mul_f32_e32 v3, 0x42800000, v5
	v_mul_f32_e32 v4, 0x42800000, v9
	v_mov_b32_e32 v5, v131
	v_cvt_pk_fp8_f32 v2, v10, v18 op_sel:[0,0,1]
	v_mul_f32_e32 v8, 0x42800000, v12
	v_mul_f32_e32 v10, 0x42800000, v20
	v_cvt_pk_fp8_f32 v5, v3, v4
	v_cvt_pk_fp8_f32 v6, v8, v10 op_sel:[0,0,1]
	s_waitcnt vmcnt(43)
	v_mul_f32_e32 v9, 0x42800000, v15
	s_waitcnt vmcnt(42)
	v_mul_f32_e32 v10, 0x42800000, v23
	v_mov_b32_e32 v11, v131
	v_cvt_pk_fp8_f32 v11, v9, v10
	v_mul_f32_e32 v3, 0x42800000, v13
	v_mul_f32_e32 v4, 0x42800000, v21
	v_cvt_pk_fp8_f32 v5, v3, v4 op_sel:[0,0,1]
	v_mul_f32_e32 v4, 0x42800000, v14
	v_mul_f32_e32 v8, 0x42800000, v22
	v_mov_b32_e32 v3, v131
	v_cvt_pk_fp8_f32 v3, v4, v8
	s_waitcnt vmcnt(41)
	v_mul_f32_e32 v4, 0x42800000, v27
	s_waitcnt vmcnt(40)
	v_mul_f32_e32 v8, 0x42800000, v35
	v_cvt_pk_fp8_f32 v11, v4, v8 op_sel:[0,0,1]
	v_mul_f32_e32 v9, 0x42800000, v17
	v_mul_f32_e32 v10, 0x42800000, v25
	v_mul_f32_e32 v4, 0x42800000, v26
	ds_write2_b32 v140, v7, v11 offset0:65 offset1:66
	v_mov_b32_e32 v11, v131
	v_cvt_pk_fp8_f32 v11, v9, v10
	v_mul_f32_e32 v8, 0x42800000, v34
	v_cvt_pk_fp8_f32 v3, v4, v8 op_sel:[0,0,1]
	v_mul_f32_e32 v4, 0x42800000, v16
	v_mul_f32_e32 v8, 0x42800000, v24
	v_mov_b32_e32 v7, v131
	v_cvt_pk_fp8_f32 v7, v4, v8
	v_mul_f32_e32 v4, 0x42800000, v29
	v_mul_f32_e32 v8, 0x42800000, v37
	v_cvt_pk_fp8_f32 v11, v4, v8 op_sel:[0,0,1]
	v_mul_f32_e32 v4, 0x42800000, v28
	v_mul_f32_e32 v8, 0x42800000, v36
	v_cvt_pk_fp8_f32 v7, v4, v8 op_sel:[0,0,1]
	ds_write2_b32 v140, v5, v11 offset0:195 offset1:196
	s_waitcnt vmcnt(39)
	v_mul_f32_e32 v5, 0x42800000, v30
	s_waitcnt vmcnt(38)
	v_mul_f32_e32 v8, 0x42800000, v38
	v_mov_b32_e32 v4, v131
	v_cvt_pk_fp8_f32 v4, v5, v8
	v_mul_f32_e32 v5, 0x42800000, v31
	v_mul_f32_e32 v8, 0x42800000, v39
	v_mov_b32_e32 v11, v131
	v_cvt_pk_fp8_f32 v11, v5, v8
	s_mov_b32 s4, s34
	s_waitcnt vmcnt(37)
	v_mul_f32_e32 v9, 0x42800000, v54
	s_waitcnt vmcnt(36)
	v_mul_f32_e32 v10, 0x42800000, v62
	v_mul_f32_e32 v5, 0x42800000, v55
	v_mul_f32_e32 v8, 0x42800000, v63
	v_cvt_pk_fp8_f32 v4, v9, v10 op_sel:[0,0,1]
	v_cvt_pk_fp8_f32 v11, v5, v8 op_sel:[0,0,1]
	v_mul_f32_e32 v5, 0x42800000, v32
	v_mul_f32_e32 v9, 0x42800000, v40
	v_mov_b32_e32 v8, v131
	s_ashr_i32 s0, s4, 31
	v_cvt_pk_fp8_f32 v8, v5, v9
	v_mul_f32_e32 v5, 0x42800000, v33
	v_mul_f32_e32 v9, 0x42800000, v41
	v_mov_b32_e32 v13, v131
	s_lshr_b32 s0, s0, 23
	v_cvt_pk_fp8_f32 v13, v5, v9
	s_add_i32 s5, s4, s0
	s_ashr_i32 s0, s5, 9
	s_ashr_i32 s1, s0, 31
	s_add_i32 s34, s34, s85
	v_mul_f32_e32 v10, 0x42800000, v56
	v_mul_f32_e32 v12, 0x42800000, v64
	v_mul_f32_e32 v5, 0x42800000, v57
	v_mul_f32_e32 v9, 0x42800000, v65
	s_lshl_b64 s[2:3], s[0:1], 25
	v_cvt_pk_fp8_f32 v8, v10, v12 op_sel:[0,0,1]
	v_cvt_pk_fp8_f32 v13, v5, v9 op_sel:[0,0,1]
	s_waitcnt vmcnt(35)
	v_mul_f32_e32 v9, 0x42800000, v50
	s_waitcnt vmcnt(34)
	v_mul_f32_e32 v10, 0x42800000, v58
	v_mov_b32_e32 v5, v131
	s_add_u32 s2, s16, s2
	v_cvt_pk_fp8_f32 v5, v9, v10
	v_mul_f32_e32 v9, 0x42800000, v51
	v_mul_f32_e32 v10, 0x42800000, v59
	v_mov_b32_e32 v15, v131
	s_addc_u32 s3, s17, s3
	s_and_b32 s5, s5, 0x7fe00
	v_cvt_pk_fp8_f32 v15, v9, v10
	s_sub_i32 s4, s4, s5
	s_lshr_b32 s4, s4, 3
	s_bfe_i32 s5, s4, 0x80000
	s_waitcnt vmcnt(33)
	v_mul_f32_e32 v12, 0x42800000, v82
	s_waitcnt vmcnt(32)
	v_mul_f32_e32 v14, 0x42800000, v90
	v_mul_f32_e32 v9, 0x42800000, v83
	v_mul_f32_e32 v10, 0x42800000, v91
	s_bfe_u32 s5, s5, 0x2000d
	v_cvt_pk_fp8_f32 v5, v12, v14 op_sel:[0,0,1]
	v_cvt_pk_fp8_f32 v15, v9, v10 op_sel:[0,0,1]
	v_mul_f32_e32 v10, 0x42800000, v52
	v_mul_f32_e32 v12, 0x42800000, v60
	v_mov_b32_e32 v9, v131
	s_add_i32 s5, s4, s5
	v_cvt_pk_fp8_f32 v9, v10, v12
	v_mul_f32_e32 v10, 0x42800000, v53
	v_mul_f32_e32 v12, 0x42800000, v61
	v_mov_b32_e32 v17, v131
	s_bfe_i32 s8, s5, 0x80000
	s_and_b32 s5, s5, 0xfc
	v_cvt_pk_fp8_f32 v17, v10, v12
	s_sub_i32 s4, s4, s5
	s_lshl_b32 s38, s0, 15
	s_sext_i32_i8 s4, s4
	s_sub_i32 s5, s35, s38
	v_mul_f32_e32 v14, 0x42800000, v84
	v_mul_f32_e32 v16, 0x42800000, v92
	s_lshl_b32 s4, s4, 9
	s_and_b32 s9, s5, 0x100
	v_cvt_pk_fp8_f32 v9, v14, v16 op_sel:[0,0,1]
	v_mul_f32_e32 v10, 0x42800000, v85
	v_mul_f32_e32 v12, 0x42800000, v93
	s_sext_i32_i16 s8, s8
	s_or_b32 s37, s4, s9
	v_cvt_pk_fp8_f32 v17, v10, v12 op_sel:[0,0,1]
	v_or_b32_e32 v134, s37, v137
	s_lshl_b32 s4, s8, 6
	ds_write_b128 v140, v[2:5]
	ds_write2_b32 v140, v11, v15 offset0:67 offset1:68
	ds_write2_b64 v140, v[6:7], v[8:9] offset0:65 offset1:66
	ds_write2_b32 v140, v13, v17 offset0:197 offset1:198
	v_or_b32_e32 v2, 0x80, v134
	s_and_b32 s36, s4, 0xffffff00
	s_and_b32 s4, s5, 0xc0
	v_ashrrev_i32_e32 v3, 31, v2
	s_or_b32 s4, s36, s4
	v_lshlrev_b64 v[2:3], 14, v[2:3]
	s_ashr_i32 s5, s4, 31
	v_lshl_add_u64 v[2:3], s[2:3], 0, v[2:3]
	s_lshl_b64 s[4:5], s[4:5], 2
	v_lshl_add_u64 v[2:3], v[2:3], 0, s[4:5]
	v_lshl_add_u64 v[82:83], v[2:3], 0, v[130:131]
	v_add_co_u32_e32 v6, vcc, s11, v82
	s_waitcnt vmcnt(31)
	v_mul_f32_e32 v135, 0x42800000, v42
	v_addc_co_u32_e32 v7, vcc, 0, v83, vcc
	v_add_co_u32_e32 v10, vcc, s18, v82
	global_load_dwordx4 v[2:5], v[82:83], off nt
	s_nop 0
	global_load_dwordx4 v[6:9], v[6:7], off nt
	v_addc_co_u32_e32 v11, vcc, 0, v83, vcc
	v_add_co_u32_e32 v14, vcc, s19, v82
	s_waitcnt vmcnt(32)
	v_mul_f32_e32 v46, 0x42800000, v46
	v_addc_co_u32_e32 v15, vcc, 0, v83, vcc
	global_load_dwordx4 v[10:13], v[10:11], off nt
	s_nop 0
	global_load_dwordx4 v[18:21], v[14:15], off nt
	v_add_co_u32_e32 v14, vcc, s20, v82
	v_mov_b32_e32 v42, v131
	s_nop 0
	v_addc_co_u32_e32 v15, vcc, 0, v83, vcc
	v_add_co_u32_e32 v22, vcc, s21, v82
	v_cvt_pk_fp8_f32 v42, v135, v46
	s_nop 0
	v_addc_co_u32_e32 v23, vcc, 0, v83, vcc
	v_add_co_u32_e32 v26, vcc, s22, v82
	v_mul_f32_e32 v43, 0x42800000, v43
	v_mul_f32_e32 v46, 0x42800000, v47
	v_mov_b32_e32 v47, v131
	v_addc_co_u32_e32 v27, vcc, 0, v83, vcc
	v_cvt_pk_fp8_f32 v47, v43, v46
	v_add_co_u32_e32 v30, vcc, s23, v82
	global_load_dwordx4 v[14:17], v[14:15], off nt
	s_nop 0
	global_load_dwordx4 v[22:25], v[22:23], off nt
	v_addc_co_u32_e32 v31, vcc, 0, v83, vcc
	global_load_dwordx4 v[26:29], v[26:27], off nt
	s_nop 0
	global_load_dwordx4 v[34:37], v[30:31], off nt
	v_add_co_u32_e32 v30, vcc, s24, v82
	s_waitcnt vmcnt(37)
	v_mul_f32_e32 v43, 0x42800000, v71
	s_waitcnt vmcnt(36)
	v_mul_f32_e32 v46, 0x42800000, v79
	v_addc_co_u32_e32 v31, vcc, 0, v83, vcc
	v_cvt_pk_fp8_f32 v47, v43, v46 op_sel:[0,0,1]
	v_mul_f32_e32 v43, 0x42800000, v44
	v_mul_f32_e32 v44, 0x42800000, v48
	v_mov_b32_e32 v46, v131
	v_add_co_u32_e32 v38, vcc, s25, v82
	v_cvt_pk_fp8_f32 v46, v43, v44
	v_mul_f32_e32 v43, 0x42800000, v45
	v_mul_f32_e32 v44, 0x42800000, v49
	v_mov_b32_e32 v45, v131
	v_addc_co_u32_e32 v39, vcc, 0, v83, vcc
	v_cvt_pk_fp8_f32 v45, v43, v44
	v_add_co_u32_e32 v50, vcc, s26, v82
	v_mul_f32_e32 v43, 0x42800000, v73
	s_nop 0
	v_addc_co_u32_e32 v51, vcc, 0, v83, vcc
	v_add_co_u32_e32 v52, vcc, s27, v82
	v_mul_f32_e32 v44, 0x42800000, v81
	s_nop 0
	v_addc_co_u32_e32 v53, vcc, 0, v83, vcc
	v_cvt_pk_fp8_f32 v45, v43, v44 op_sel:[0,0,1]
	s_waitcnt vmcnt(35)
	v_mul_f32_e32 v44, 0x42800000, v66
	v_mul_f32_e32 v49, 0x42800000, v67
	s_waitcnt vmcnt(34)
	v_mul_f32_e32 v66, 0x42800000, v75
	v_mov_b32_e32 v67, v131
	global_load_dwordx4 v[30:33], v[30:31], off nt
	s_nop 0
	global_load_dwordx4 v[38:41], v[38:39], off nt
	s_nop 0
	global_load_dwordx4 v[54:57], v[50:51], off nt
	global_load_dwordx4 v[62:65], v[52:53], off nt
	v_add_co_u32_e32 v50, vcc, s28, v82
	v_mul_f32_e32 v70, 0x42800000, v70
	v_mul_f32_e32 v78, 0x42800000, v78
	v_cvt_pk_fp8_f32 v67, v49, v66
	v_addc_co_u32_e32 v51, vcc, 0, v83, vcc
	v_cvt_pk_fp8_f32 v42, v70, v78 op_sel:[0,0,1]
	v_mul_f32_e32 v48, 0x42800000, v72
	v_mul_f32_e32 v70, 0x42800000, v80
	v_add_co_u32_e32 v58, vcc, s29, v82
	v_cvt_pk_fp8_f32 v46, v48, v70 op_sel:[0,0,1]
	v_mul_f32_e32 v48, 0x42800000, v74
	v_mov_b32_e32 v43, v131
	v_addc_co_u32_e32 v59, vcc, 0, v83, vcc
	v_cvt_pk_fp8_f32 v43, v44, v48
	s_waitcnt vmcnt(37)
	v_mul_f32_e32 v44, 0x42800000, v87
	s_waitcnt vmcnt(36)
	v_mul_f32_e32 v48, 0x42800000, v99
	v_add_co_u32_e32 v84, vcc, s30, v82
	v_cvt_pk_fp8_f32 v67, v44, v48 op_sel:[0,0,1]
	s_nop 0
	v_addc_co_u32_e32 v85, vcc, 0, v83, vcc
	v_add_co_u32_e32 v90, vcc, s31, v82
	global_load_dwordx4 v[50:53], v[50:51], off nt
	s_nop 0
	global_load_dwordx4 v[58:61], v[58:59], off nt
	v_addc_co_u32_e32 v91, vcc, 0, v83, vcc
	global_load_dwordx4 v[82:85], v[84:85], off nt
	s_nop 0
	global_load_dwordx4 v[90:93], v[90:91], off nt
	ds_write2_b32 v142, v47, v67 offset0:81 offset1:82
	v_mul_f32_e32 v49, 0x42800000, v69
	v_mul_f32_e32 v66, 0x42800000, v77
	v_mov_b32_e32 v67, v131
	v_cvt_pk_fp8_f32 v67, v49, v66
	v_mul_f32_e32 v44, 0x42800000, v86
	v_mul_f32_e32 v48, 0x42800000, v98
	v_cvt_pk_fp8_f32 v43, v44, v48 op_sel:[0,0,1]
	v_mul_f32_e32 v44, 0x42800000, v68
	v_mul_f32_e32 v48, 0x42800000, v76
	v_mov_b32_e32 v47, v131
	v_cvt_pk_fp8_f32 v47, v44, v48
	v_mul_f32_e32 v44, 0x42800000, v89
	v_mul_f32_e32 v48, 0x42800000, v101
	v_cvt_pk_fp8_f32 v67, v44, v48 op_sel:[0,0,1]
	v_mul_f32_e32 v44, 0x42800000, v88
	v_mul_f32_e32 v48, 0x42800000, v100
	v_cvt_pk_fp8_f32 v47, v44, v48 op_sel:[0,0,1]
	ds_write2_b32 v142, v45, v67 offset0:211 offset1:212
	s_waitcnt vmcnt(39)
	v_mul_f32_e32 v45, 0x42800000, v94
	s_waitcnt vmcnt(38)
	v_mul_f32_e32 v48, 0x42800000, v102
	v_mov_b32_e32 v44, v131
	v_cvt_pk_fp8_f32 v44, v45, v48
	v_mul_f32_e32 v45, 0x42800000, v95
	v_mul_f32_e32 v48, 0x42800000, v103
	v_mov_b32_e32 v67, v131
	v_cvt_pk_fp8_f32 v67, v45, v48
	s_waitcnt vmcnt(37)
	v_mul_f32_e32 v49, 0x42800000, v110
	s_waitcnt vmcnt(36)
	v_mul_f32_e32 v66, 0x42800000, v118
	v_mul_f32_e32 v45, 0x42800000, v111
	v_mul_f32_e32 v48, 0x42800000, v119
	v_cvt_pk_fp8_f32 v44, v49, v66 op_sel:[0,0,1]
	v_cvt_pk_fp8_f32 v67, v45, v48 op_sel:[0,0,1]
	v_mul_f32_e32 v45, 0x42800000, v96
	v_mul_f32_e32 v49, 0x42800000, v104
	v_mov_b32_e32 v48, v131
	v_cvt_pk_fp8_f32 v48, v45, v49
	v_mul_f32_e32 v45, 0x42800000, v97
	v_mul_f32_e32 v49, 0x42800000, v105
	v_mov_b32_e32 v69, v131
	v_cvt_pk_fp8_f32 v69, v45, v49
	v_mul_f32_e32 v66, 0x42800000, v112
	v_mul_f32_e32 v68, 0x42800000, v120
	v_mul_f32_e32 v45, 0x42800000, v113
	v_mul_f32_e32 v49, 0x42800000, v121
	v_cvt_pk_fp8_f32 v48, v66, v68 op_sel:[0,0,1]
	v_cvt_pk_fp8_f32 v69, v45, v49 op_sel:[0,0,1]
	s_waitcnt vmcnt(35)
	v_mul_f32_e32 v49, 0x42800000, v106
	s_waitcnt vmcnt(34)
	v_mul_f32_e32 v66, 0x42800000, v114
	v_mov_b32_e32 v45, v131
	v_cvt_pk_fp8_f32 v45, v49, v66
	v_mul_f32_e32 v49, 0x42800000, v107
	v_mul_f32_e32 v66, 0x42800000, v115
	v_mov_b32_e32 v71, v131
	v_cvt_pk_fp8_f32 v71, v49, v66
	s_waitcnt vmcnt(33)
	v_mul_f32_e32 v68, 0x42800000, v122
	s_waitcnt vmcnt(32)
	v_mul_f32_e32 v70, 0x42800000, v126
	v_mul_f32_e32 v49, 0x42800000, v123
	v_mul_f32_e32 v66, 0x42800000, v127
	v_cvt_pk_fp8_f32 v45, v68, v70 op_sel:[0,0,1]
	v_cvt_pk_fp8_f32 v71, v49, v66 op_sel:[0,0,1]
	v_mul_f32_e32 v66, 0x42800000, v108
	v_mul_f32_e32 v68, 0x42800000, v116
	v_mov_b32_e32 v49, v131
	v_cvt_pk_fp8_f32 v49, v66, v68
	v_mul_f32_e32 v66, 0x42800000, v109
	v_mul_f32_e32 v68, 0x42800000, v117
	v_mov_b32_e32 v73, v131
	v_cvt_pk_fp8_f32 v73, v66, v68
	v_mul_f32_e32 v70, 0x42800000, v124
	v_mul_f32_e32 v72, 0x42800000, v128
	v_cvt_pk_fp8_f32 v49, v70, v72 op_sel:[0,0,1]
	v_mul_f32_e32 v66, 0x42800000, v125
	v_mul_f32_e32 v68, 0x42800000, v129
	v_cvt_pk_fp8_f32 v73, v66, v68 op_sel:[0,0,1]
	ds_write_b128 v142, v[42:45] offset:64
	ds_write2_b32 v142, v67, v71 offset0:83 offset1:84
	ds_write2_b64 v142, v[46:47], v[48:49] offset0:73 offset1:74
	ds_write2_b32 v142, v69, v73 offset0:213 offset1:214
	v_or_b32_e32 v42, 0xc0, v134
	v_ashrrev_i32_e32 v43, 31, v42
	v_lshlrev_b64 v[42:43], 14, v[42:43]
	v_lshl_add_u64 v[42:43], s[2:3], 0, v[42:43]
	v_lshl_add_u64 v[42:43], v[42:43], 0, s[4:5]
	v_lshl_add_u64 v[122:123], v[42:43], 0, v[130:131]
	v_add_co_u32_e32 v46, vcc, s11, v122
	s_waitcnt vmcnt(15)
	v_mul_f32_e32 v134, 0x42800000, v2
	v_addc_co_u32_e32 v47, vcc, 0, v123, vcc
	v_add_co_u32_e32 v66, vcc, s18, v122
	global_load_dwordx4 v[42:45], v[122:123], off nt
	s_nop 0
	global_load_dwordx4 v[46:49], v[46:47], off nt
	v_addc_co_u32_e32 v67, vcc, 0, v123, vcc
	v_add_co_u32_e32 v68, vcc, s19, v122
	s_waitcnt vmcnt(16)
	v_mul_f32_e32 v135, 0x42800000, v6
	v_addc_co_u32_e32 v69, vcc, 0, v123, vcc
	global_load_dwordx4 v[70:73], v[66:67], off nt
	global_load_dwordx4 v[78:81], v[68:69], off nt
	v_add_co_u32_e32 v66, vcc, s20, v122
	v_mov_b32_e32 v144, v131
	s_nop 0
	v_addc_co_u32_e32 v67, vcc, 0, v123, vcc
	v_add_co_u32_e32 v74, vcc, s21, v122
	v_cvt_pk_fp8_f32 v144, v134, v135
	s_nop 0
	v_addc_co_u32_e32 v75, vcc, 0, v123, vcc
	v_add_co_u32_e32 v86, vcc, s22, v122
	global_load_dwordx4 v[66:69], v[66:67], off nt
	s_nop 0
	global_load_dwordx4 v[74:77], v[74:75], off nt
	v_addc_co_u32_e32 v87, vcc, 0, v123, vcc
	v_add_co_u32_e32 v94, vcc, s23, v122
	v_mul_f32_e32 v134, 0x42800000, v3
	s_nop 0
	v_addc_co_u32_e32 v95, vcc, 0, v123, vcc
	global_load_dwordx4 v[86:89], v[86:87], off nt
	s_nop 0
	global_load_dwordx4 v[98:101], v[94:95], off nt
	v_add_co_u32_e32 v94, vcc, s24, v122
	v_mul_f32_e32 v135, 0x42800000, v7
	s_nop 0
	v_addc_co_u32_e32 v95, vcc, 0, v123, vcc
	v_add_co_u32_e32 v102, vcc, s25, v122
	v_mov_b32_e32 v146, v131
	s_nop 0
	v_addc_co_u32_e32 v103, vcc, 0, v123, vcc
	v_add_co_u32_e32 v106, vcc, s26, v122
	global_load_dwordx4 v[94:97], v[94:95], off nt
	s_nop 0
	global_load_dwordx4 v[102:105], v[102:103], off nt
	v_addc_co_u32_e32 v107, vcc, 0, v123, vcc
	v_add_co_u32_e32 v108, vcc, s27, v122
	v_cvt_pk_fp8_f32 v146, v134, v135
	s_nop 0
	v_addc_co_u32_e32 v109, vcc, 0, v123, vcc
	global_load_dwordx4 v[110:113], v[106:107], off nt
	global_load_dwordx4 v[118:121], v[108:109], off nt
	v_add_co_u32_e32 v106, vcc, s28, v122
	s_waitcnt vmcnt(25)
	v_mul_f32_e32 v143, 0x42800000, v10
	v_addc_co_u32_e32 v107, vcc, 0, v123, vcc
	v_add_co_u32_e32 v114, vcc, s29, v122
	s_waitcnt vmcnt(24)
	v_mul_f32_e32 v145, 0x42800000, v18
	v_addc_co_u32_e32 v115, vcc, 0, v123, vcc
	v_add_co_u32_e32 v124, vcc, s30, v122
	global_load_dwordx4 v[106:109], v[106:107], off nt
	s_nop 0
	global_load_dwordx4 v[114:117], v[114:115], off nt
	v_addc_co_u32_e32 v125, vcc, 0, v123, vcc
	v_add_co_u32_e32 v126, vcc, s31, v122
	v_mul_f32_e32 v134, 0x42800000, v11
	s_nop 0
	v_addc_co_u32_e32 v127, vcc, 0, v123, vcc
	global_load_dwordx4 v[122:125], v[124:125], off nt
	s_nop 0
	global_load_dwordx4 v[126:129], v[126:127], off nt
	v_mul_f32_e32 v135, 0x42800000, v19
	v_cvt_pk_fp8_f32 v144, v143, v145 op_sel:[0,0,1]
	v_cvt_pk_fp8_f32 v146, v134, v135 op_sel:[0,0,1]
	v_mul_f32_e32 v135, 0x42800000, v4
	v_mul_f32_e32 v143, 0x42800000, v8
	v_mov_b32_e32 v134, v131
	v_cvt_pk_fp8_f32 v134, v135, v143
	v_mul_f32_e32 v135, 0x42800000, v5
	v_mul_f32_e32 v143, 0x42800000, v9
	v_mov_b32_e32 v148, v131
	v_mul_f32_e32 v145, 0x42800000, v12
	v_mul_f32_e32 v147, 0x42800000, v20
	v_cvt_pk_fp8_f32 v148, v135, v143
	v_cvt_pk_fp8_f32 v134, v145, v147 op_sel:[0,0,1]
	s_waitcnt vmcnt(27)
	v_mul_f32_e32 v147, 0x42800000, v15
	s_waitcnt vmcnt(26)
	v_mul_f32_e32 v149, 0x42800000, v23
	v_mov_b32_e32 v150, v131
	v_cvt_pk_fp8_f32 v150, v147, v149
	v_mul_f32_e32 v135, 0x42800000, v13
	v_mul_f32_e32 v143, 0x42800000, v21
	v_cvt_pk_fp8_f32 v148, v135, v143 op_sel:[0,0,1]
	v_mul_f32_e32 v135, 0x42800000, v14
	v_mul_f32_e32 v143, 0x42800000, v22
	v_mov_b32_e32 v145, v131
	v_cvt_pk_fp8_f32 v145, v135, v143
	s_waitcnt vmcnt(25)
	v_mul_f32_e32 v135, 0x42800000, v27
	s_waitcnt vmcnt(24)
	v_mul_f32_e32 v143, 0x42800000, v35
	v_cvt_pk_fp8_f32 v150, v135, v143 op_sel:[0,0,1]
	v_mul_f32_e32 v147, 0x42800000, v17
	v_mul_f32_e32 v149, 0x42800000, v25
	v_mul_f32_e32 v135, 0x42800000, v26
	ds_write2_b32 v142, v146, v150 offset0:97 offset1:98
	v_mov_b32_e32 v150, v131
	v_cvt_pk_fp8_f32 v150, v147, v149
	v_mul_f32_e32 v143, 0x42800000, v34
	v_cvt_pk_fp8_f32 v145, v135, v143 op_sel:[0,0,1]
	v_mul_f32_e32 v143, 0x42800000, v16
	v_mul_f32_e32 v146, 0x42800000, v24
	v_mov_b32_e32 v135, v131
	v_cvt_pk_fp8_f32 v135, v143, v146
	v_mul_f32_e32 v143, 0x42800000, v29
	v_mul_f32_e32 v146, 0x42800000, v37
	v_cvt_pk_fp8_f32 v150, v143, v146 op_sel:[0,0,1]
	v_mul_f32_e32 v143, 0x42800000, v28
	v_mul_f32_e32 v146, 0x42800000, v36
	v_cvt_pk_fp8_f32 v135, v143, v146 op_sel:[0,0,1]
	s_waitcnt vmcnt(23)
	v_mul_f32_e32 v143, 0x42800000, v30
	s_waitcnt vmcnt(22)
	v_mul_f32_e32 v147, 0x42800000, v38
	v_mov_b32_e32 v146, v131
	ds_write2_b32 v142, v148, v150 offset0:227 offset1:228
	v_cvt_pk_fp8_f32 v146, v143, v147
	v_mul_f32_e32 v143, 0x42800000, v31
	v_mul_f32_e32 v147, 0x42800000, v39
	v_mov_b32_e32 v150, v131
	v_cvt_pk_fp8_f32 v150, v143, v147
	s_waitcnt vmcnt(21)
	v_mul_f32_e32 v148, 0x42800000, v54
	s_waitcnt vmcnt(20)
	v_mul_f32_e32 v149, 0x42800000, v62
	v_mul_f32_e32 v143, 0x42800000, v55
	v_mul_f32_e32 v147, 0x42800000, v63
	v_cvt_pk_fp8_f32 v146, v148, v149 op_sel:[0,0,1]
	v_cvt_pk_fp8_f32 v150, v143, v147 op_sel:[0,0,1]
	v_mul_f32_e32 v143, 0x42800000, v32
	v_mul_f32_e32 v147, 0x42800000, v40
	v_mov_b32_e32 v148, v131
	v_cvt_pk_fp8_f32 v148, v143, v147
	v_mul_f32_e32 v143, 0x42800000, v33
	v_mul_f32_e32 v147, 0x42800000, v41
	v_mov_b32_e32 v152, v131
	v_cvt_pk_fp8_f32 v152, v143, v147
	v_mul_f32_e32 v149, 0x42800000, v56
	v_mul_f32_e32 v151, 0x42800000, v64
	v_mul_f32_e32 v143, 0x42800000, v57
	v_mul_f32_e32 v147, 0x42800000, v65
	v_cvt_pk_fp8_f32 v148, v149, v151 op_sel:[0,0,1]
	v_cvt_pk_fp8_f32 v152, v143, v147 op_sel:[0,0,1]
	s_waitcnt vmcnt(19)
	v_mul_f32_e32 v143, 0x42800000, v50
	s_waitcnt vmcnt(18)
	v_mul_f32_e32 v149, 0x42800000, v58
	v_mov_b32_e32 v147, v131
	v_cvt_pk_fp8_f32 v147, v143, v149
	v_mul_f32_e32 v143, 0x42800000, v51
	v_mul_f32_e32 v149, 0x42800000, v59
	v_mov_b32_e32 v154, v131
	v_cvt_pk_fp8_f32 v154, v143, v149
	s_waitcnt vmcnt(17)
	v_mul_f32_e32 v151, 0x42800000, v82
	s_waitcnt vmcnt(16)
	v_mul_f32_e32 v153, 0x42800000, v90
	v_mul_f32_e32 v143, 0x42800000, v83
	v_mul_f32_e32 v149, 0x42800000, v91
	v_cvt_pk_fp8_f32 v147, v151, v153 op_sel:[0,0,1]
	v_cvt_pk_fp8_f32 v154, v143, v149 op_sel:[0,0,1]
	v_mul_f32_e32 v143, 0x42800000, v52
	v_mul_f32_e32 v151, 0x42800000, v60
	v_mov_b32_e32 v149, v131
	v_cvt_pk_fp8_f32 v149, v143, v151
	v_mul_f32_e32 v143, 0x42800000, v53
	v_mul_f32_e32 v151, 0x42800000, v61
	v_mov_b32_e32 v156, v131
	v_cvt_pk_fp8_f32 v156, v143, v151
	v_mul_f32_e32 v153, 0x42800000, v84
	v_mul_f32_e32 v155, 0x42800000, v92
	s_cmpk_gt_i32 s34, 0x3fff
	v_cvt_pk_fp8_f32 v149, v153, v155 op_sel:[0,0,1]
	v_mul_f32_e32 v143, 0x42800000, v85
	v_mul_f32_e32 v151, 0x42800000, v93
	s_cselect_b64 s[2:3], -1, 0
	v_cvt_pk_fp8_f32 v156, v143, v151 op_sel:[0,0,1]
	s_and_b64 vcc, exec, s[2:3]
	ds_write_b128 v142, v[144:147] offset:128
	ds_write2_b32 v142, v150, v154 offset0:99 offset1:100
	ds_write2_b64 v142, v[134:135], v[148:149] offset0:81 offset1:82
	ds_write2_b32 v142, v152, v156 offset0:229 offset1:230
	s_cbranch_vccz .Lcv1_a
	s_waitcnt vmcnt(0)
	s_branch .LBB0_223
.Lcv1_a:
	s_ashr_i32 s4, s34, 31
	s_lshr_b32 s4, s4, 23
	s_add_i32 s8, s34, s4
	s_ashr_i32 s4, s8, 9
	s_ashr_i32 s5, s4, 31
	s_lshl_b64 s[4:5], s[4:5], 25
	s_add_u32 s4, s16, s4
	s_addc_u32 s5, s17, s5
	s_and_b32 s8, s8, 0xfffffe00
	s_sub_i32 s8, s34, s8
	s_lshr_b32 s9, s8, 3
	s_bfe_i32 s39, s9, 0x80000
	s_bfe_u32 s39, s39, 0x2000d
	s_add_i32 s39, s9, s39
	s_bfe_i32 s40, s39, 0x80000
	s_and_b32 s39, s39, 0xfc
	s_sub_i32 s9, s9, s39
	s_sext_i32_i8 s9, s9
	s_lshl_b32 s8, s8, 6
	s_lshl_b32 s9, s9, 9
	s_and_b32 s39, s8, 0x100
	s_or_b32 s9, s9, s39
	v_or_b32_e32 v2, s9, v137
	v_ashrrev_i32_e32 v3, 31, v2
	s_sext_i32_i16 s40, s40
	v_lshlrev_b64 v[2:3], 14, v[2:3]
	v_lshl_add_u64 v[2:3], s[4:5], 0, v[2:3]
	s_lshl_b32 s4, s40, 6
	s_and_b32 s4, s4, 0xffffff00
	s_and_b32 s5, s8, 0xc0
	s_or_b32 s4, s4, s5
	s_ashr_i32 s5, s4, 31
	v_lshl_add_u64 v[2:3], s[4:5], 2, v[2:3]
	v_lshl_add_u64 v[82:83], v[2:3], 0, v[130:131]
	v_add_co_u32_e32 v6, vcc, s11, v82
	s_nop 1
	v_addc_co_u32_e32 v7, vcc, 0, v83, vcc
	v_add_co_u32_e32 v10, vcc, s18, v82
	global_load_dwordx4 v[2:5], v[82:83], off nt
	s_nop 0
	global_load_dwordx4 v[6:9], v[6:7], off nt
	v_addc_co_u32_e32 v11, vcc, 0, v83, vcc
	v_add_co_u32_e32 v14, vcc, s19, v82
	s_nop 1
	v_addc_co_u32_e32 v15, vcc, 0, v83, vcc
	global_load_dwordx4 v[10:13], v[10:11], off nt
	s_nop 0
	global_load_dwordx4 v[18:21], v[14:15], off nt
	v_add_co_u32_e32 v14, vcc, s20, v82
	s_nop 1
	v_addc_co_u32_e32 v15, vcc, 0, v83, vcc
	v_add_co_u32_e32 v22, vcc, s21, v82
	s_nop 1
	v_addc_co_u32_e32 v23, vcc, 0, v83, vcc
	v_add_co_u32_e32 v26, vcc, s22, v82
	global_load_dwordx4 v[14:17], v[14:15], off nt
	s_nop 0
	global_load_dwordx4 v[22:25], v[22:23], off nt
	v_addc_co_u32_e32 v27, vcc, 0, v83, vcc
	v_add_co_u32_e32 v30, vcc, s23, v82
	s_nop 1
	v_addc_co_u32_e32 v31, vcc, 0, v83, vcc
	global_load_dwordx4 v[26:29], v[26:27], off nt
	s_nop 0
	global_load_dwordx4 v[34:37], v[30:31], off nt
	v_add_co_u32_e32 v30, vcc, s24, v82
	s_nop 1
	v_addc_co_u32_e32 v31, vcc, 0, v83, vcc
	v_add_co_u32_e32 v38, vcc, s25, v82
	s_nop 1
	v_addc_co_u32_e32 v39, vcc, 0, v83, vcc
	v_add_co_u32_e32 v50, vcc, s26, v82
	global_load_dwordx4 v[30:33], v[30:31], off nt
	s_nop 0
	global_load_dwordx4 v[38:41], v[38:39], off nt
	v_addc_co_u32_e32 v51, vcc, 0, v83, vcc
	v_add_co_u32_e32 v52, vcc, s27, v82
	s_nop 1
	v_addc_co_u32_e32 v53, vcc, 0, v83, vcc
	global_load_dwordx4 v[54:57], v[50:51], off nt
	global_load_dwordx4 v[62:65], v[52:53], off nt
	v_add_co_u32_e32 v50, vcc, 0x30000, v82
	s_nop 1
	v_addc_co_u32_e32 v51, vcc, 0, v83, vcc
	v_add_co_u32_e32 v58, vcc, 0x34000, v82
	s_nop 1
	v_addc_co_u32_e32 v59, vcc, 0, v83, vcc
	v_add_co_u32_e32 v84, vcc, 0x38000, v82
	global_load_dwordx4 v[50:53], v[50:51], off nt
	s_nop 0
	global_load_dwordx4 v[58:61], v[58:59], off nt
	v_addc_co_u32_e32 v85, vcc, 0, v83, vcc
	v_add_co_u32_e32 v90, vcc, 0x3c000, v82
	s_nop 1
	v_addc_co_u32_e32 v91, vcc, 0, v83, vcc
	global_load_dwordx4 v[82:85], v[84:85], off nt
	s_nop 0
	global_load_dwordx4 v[90:93], v[90:91], off nt
.LBB0_223:
	s_waitcnt vmcnt(31)
	v_mul_f32_e32 v134, 0x42800000, v42
	s_waitcnt vmcnt(30)
	v_mul_f32_e32 v135, 0x42800000, v46
	v_mov_b32_e32 v144, v131
	v_cvt_pk_fp8_f32 v144, v134, v135
	v_mul_f32_e32 v134, 0x42800000, v43
	v_mul_f32_e32 v135, 0x42800000, v47
	v_mov_b32_e32 v146, v131
	v_cvt_pk_fp8_f32 v146, v134, v135
	s_waitcnt vmcnt(29)
	v_mul_f32_e32 v143, 0x42800000, v70
	s_waitcnt vmcnt(28)
	v_mul_f32_e32 v145, 0x42800000, v78
	v_mul_f32_e32 v134, 0x42800000, v71
	v_mul_f32_e32 v135, 0x42800000, v79
	v_cvt_pk_fp8_f32 v144, v143, v145 op_sel:[0,0,1]
	v_cvt_pk_fp8_f32 v146, v134, v135 op_sel:[0,0,1]
	v_mul_f32_e32 v135, 0x42800000, v44
	v_mul_f32_e32 v143, 0x42800000, v48
	v_mov_b32_e32 v134, v131
	v_cvt_pk_fp8_f32 v134, v135, v143
	v_mul_f32_e32 v135, 0x42800000, v45
	v_mul_f32_e32 v143, 0x42800000, v49
	v_mov_b32_e32 v148, v131
	v_mul_f32_e32 v145, 0x42800000, v72
	v_mul_f32_e32 v147, 0x42800000, v80
	v_cvt_pk_fp8_f32 v148, v135, v143
	v_cvt_pk_fp8_f32 v134, v145, v147 op_sel:[0,0,1]
	s_waitcnt vmcnt(27)
	v_mul_f32_e32 v147, 0x42800000, v67
	s_waitcnt vmcnt(26)
	v_mul_f32_e32 v149, 0x42800000, v75
	v_mov_b32_e32 v150, v131
	v_cvt_pk_fp8_f32 v150, v147, v149
	v_mul_f32_e32 v135, 0x42800000, v73
	v_mul_f32_e32 v143, 0x42800000, v81
	v_cvt_pk_fp8_f32 v148, v135, v143 op_sel:[0,0,1]
	v_mul_f32_e32 v135, 0x42800000, v66
	v_mul_f32_e32 v143, 0x42800000, v74
	v_mov_b32_e32 v145, v131
	v_cvt_pk_fp8_f32 v145, v135, v143
	s_waitcnt vmcnt(25)
	v_mul_f32_e32 v135, 0x42800000, v87
	s_waitcnt vmcnt(24)
	v_mul_f32_e32 v143, 0x42800000, v99
	v_cvt_pk_fp8_f32 v150, v135, v143 op_sel:[0,0,1]
	v_mul_f32_e32 v147, 0x42800000, v69
	v_mul_f32_e32 v149, 0x42800000, v77
	v_mul_f32_e32 v135, 0x42800000, v86
	ds_write2_b32 v142, v146, v150 offset0:113 offset1:114
	v_mov_b32_e32 v150, v131
	v_cvt_pk_fp8_f32 v150, v147, v149
	v_mul_f32_e32 v143, 0x42800000, v98
	v_cvt_pk_fp8_f32 v145, v135, v143 op_sel:[0,0,1]
	v_mul_f32_e32 v143, 0x42800000, v68
	v_mul_f32_e32 v146, 0x42800000, v76
	v_mov_b32_e32 v135, v131
	v_cvt_pk_fp8_f32 v135, v143, v146
	v_mul_f32_e32 v143, 0x42800000, v89
	v_mul_f32_e32 v146, 0x42800000, v101
	v_cvt_pk_fp8_f32 v150, v143, v146 op_sel:[0,0,1]
	v_mul_f32_e32 v143, 0x42800000, v88
	v_mul_f32_e32 v146, 0x42800000, v100
	v_cvt_pk_fp8_f32 v135, v143, v146 op_sel:[0,0,1]
	s_waitcnt vmcnt(23)
	v_mul_f32_e32 v143, 0x42800000, v94
	s_waitcnt vmcnt(22)
	v_mul_f32_e32 v147, 0x42800000, v102
	v_mov_b32_e32 v146, v131
	ds_write2_b32 v142, v148, v150 offset0:243 offset1:244
	v_cvt_pk_fp8_f32 v146, v143, v147
	v_mul_f32_e32 v143, 0x42800000, v95
	v_mul_f32_e32 v147, 0x42800000, v103
	v_mov_b32_e32 v150, v131
	v_cvt_pk_fp8_f32 v150, v143, v147
	s_waitcnt vmcnt(21)
	v_mul_f32_e32 v148, 0x42800000, v110
	s_waitcnt vmcnt(20)
	v_mul_f32_e32 v149, 0x42800000, v118
	v_mul_f32_e32 v143, 0x42800000, v111
	v_mul_f32_e32 v147, 0x42800000, v119
	v_cvt_pk_fp8_f32 v146, v148, v149 op_sel:[0,0,1]
	v_cvt_pk_fp8_f32 v150, v143, v147 op_sel:[0,0,1]
	v_mul_f32_e32 v143, 0x42800000, v96
	v_mul_f32_e32 v147, 0x42800000, v104
	v_mov_b32_e32 v148, v131
	v_cvt_pk_fp8_f32 v148, v143, v147
	v_mul_f32_e32 v143, 0x42800000, v97
	v_mul_f32_e32 v147, 0x42800000, v105
	v_mov_b32_e32 v152, v131
	v_cvt_pk_fp8_f32 v152, v143, v147
	v_mul_f32_e32 v149, 0x42800000, v112
	v_mul_f32_e32 v151, 0x42800000, v120
	v_mul_f32_e32 v143, 0x42800000, v113
	v_mul_f32_e32 v147, 0x42800000, v121
	v_cvt_pk_fp8_f32 v148, v149, v151 op_sel:[0,0,1]
	v_cvt_pk_fp8_f32 v152, v143, v147 op_sel:[0,0,1]
	s_waitcnt vmcnt(19)
	v_mul_f32_e32 v143, 0x42800000, v106
	s_waitcnt vmcnt(18)
	v_mul_f32_e32 v149, 0x42800000, v114
	v_mov_b32_e32 v147, v131
	v_cvt_pk_fp8_f32 v147, v143, v149
	v_mul_f32_e32 v143, 0x42800000, v107
	v_mul_f32_e32 v149, 0x42800000, v115
	v_mov_b32_e32 v154, v131
	v_cvt_pk_fp8_f32 v154, v143, v149
	s_waitcnt vmcnt(17)
	v_mul_f32_e32 v151, 0x42800000, v122
	s_waitcnt vmcnt(16)
	v_mul_f32_e32 v153, 0x42800000, v126
	v_mul_f32_e32 v143, 0x42800000, v123
	v_mul_f32_e32 v149, 0x42800000, v127
	v_cvt_pk_fp8_f32 v147, v151, v153 op_sel:[0,0,1]
	v_cvt_pk_fp8_f32 v154, v143, v149 op_sel:[0,0,1]
	v_mul_f32_e32 v143, 0x42800000, v108
	v_mul_f32_e32 v151, 0x42800000, v116
	v_mov_b32_e32 v149, v131
	v_cvt_pk_fp8_f32 v149, v143, v151
	v_mul_f32_e32 v143, 0x42800000, v109
	v_mul_f32_e32 v151, 0x42800000, v117
	v_mov_b32_e32 v156, v131
	v_cvt_pk_fp8_f32 v156, v143, v151
	v_mul_f32_e32 v153, 0x42800000, v124
	v_mul_f32_e32 v155, 0x42800000, v128
	v_cvt_pk_fp8_f32 v149, v153, v155 op_sel:[0,0,1]
	v_mul_f32_e32 v143, 0x42800000, v125
	v_mul_f32_e32 v151, 0x42800000, v129
	v_cvt_pk_fp8_f32 v156, v143, v151 op_sel:[0,0,1]
	ds_write_b128 v142, v[144:147] offset:192
	ds_write2_b32 v142, v150, v154 offset0:115 offset1:116
	ds_write2_b64 v142, v[134:135], v[148:149] offset0:89 offset1:90
	ds_write2_b32 v142, v152, v156 offset0:245 offset1:246
	v_cndmask_b32_e64 v134, 0, 1, s[2:3]
	v_cmp_ne_u32_e64 s[8:9], 1, v134
	s_andn2_b64 vcc, exec, s[2:3]
	s_mov_b64 s[2:3], -1
	s_cbranch_vccnz .LBB0_225
	s_add_i32 s4, s35, s33
	s_mov_b64 s[2:3], 0
.LBB0_225:
	s_lshl_b64 s[0:1], s[0:1], 23
	s_andn2_b64 vcc, exec, s[2:3]
	s_sub_i32 s2, 0, s38
	s_cbranch_vccz .Lcv1_b
	s_waitcnt vmcnt(0)
	s_branch .LBB0_220
.Lcv1_b:
	s_ashr_i32 s3, s34, 31
	s_lshr_b32 s3, s3, 23
	s_add_i32 s3, s34, s3
	s_ashr_i32 s38, s3, 9
	s_ashr_i32 s39, s38, 31
	s_lshl_b64 s[4:5], s[38:39], 25
	s_add_u32 s40, s16, s4
	s_addc_u32 s41, s17, s5
	s_and_b32 s3, s3, 0x7fe00
	s_sub_i32 s3, s34, s3
	s_lshr_b32 s3, s3, 3
	s_bfe_i32 s4, s3, 0x80000
	s_bfe_u32 s4, s4, 0x2000d
	s_add_i32 s4, s3, s4
	s_bfe_i32 s5, s4, 0x80000
	s_and_b32 s4, s4, 0xfc
	s_sub_i32 s3, s3, s4
	s_add_i32 s4, s33, s35
	s_lshl_b32 s38, s38, 15
	s_sext_i32_i8 s3, s3
	s_sub_i32 s38, s4, s38
	s_lshl_b32 s3, s3, 9
	s_and_b32 s39, s38, 0x100
	s_sext_i32_i16 s5, s5
	s_or_b32 s3, s3, s39
	v_or_b32_e32 v42, s3, v138
	s_lshl_b32 s3, s5, 6
	v_ashrrev_i32_e32 v43, 31, v42
	s_and_b32 s3, s3, 0xffffff00
	s_and_b32 s5, s38, 0xc0
	v_lshlrev_b64 v[42:43], 14, v[42:43]
	s_or_b32 s38, s3, s5
	v_lshl_add_u64 v[42:43], s[40:41], 0, v[42:43]
	s_ashr_i32 s39, s38, 31
	v_lshl_add_u64 v[42:43], s[38:39], 2, v[42:43]
	v_lshl_add_u64 v[122:123], v[42:43], 0, v[130:131]
	v_add_co_u32_e32 v46, vcc, s11, v122
	s_nop 1
	v_addc_co_u32_e32 v47, vcc, 0, v123, vcc
	v_add_co_u32_e32 v66, vcc, s18, v122
	global_load_dwordx4 v[42:45], v[122:123], off nt
	s_nop 0
	global_load_dwordx4 v[46:49], v[46:47], off nt
	v_addc_co_u32_e32 v67, vcc, 0, v123, vcc
	v_add_co_u32_e32 v68, vcc, s19, v122
	s_nop 1
	v_addc_co_u32_e32 v69, vcc, 0, v123, vcc
	global_load_dwordx4 v[70:73], v[66:67], off nt
	global_load_dwordx4 v[78:81], v[68:69], off nt
	v_add_co_u32_e32 v66, vcc, s20, v122
	s_nop 1
	v_addc_co_u32_e32 v67, vcc, 0, v123, vcc
	v_add_co_u32_e32 v74, vcc, s21, v122
	s_nop 1
	v_addc_co_u32_e32 v75, vcc, 0, v123, vcc
	v_add_co_u32_e32 v86, vcc, s22, v122
	global_load_dwordx4 v[66:69], v[66:67], off nt
	s_nop 0
	global_load_dwordx4 v[74:77], v[74:75], off nt
	v_addc_co_u32_e32 v87, vcc, 0, v123, vcc
	v_add_co_u32_e32 v94, vcc, s23, v122
	s_nop 1
	v_addc_co_u32_e32 v95, vcc, 0, v123, vcc
	global_load_dwordx4 v[86:89], v[86:87], off nt
	s_nop 0
	global_load_dwordx4 v[98:101], v[94:95], off nt
	v_add_co_u32_e32 v94, vcc, s24, v122
	s_nop 1
	v_addc_co_u32_e32 v95, vcc, 0, v123, vcc
	v_add_co_u32_e32 v102, vcc, s25, v122
	s_nop 1
	v_addc_co_u32_e32 v103, vcc, 0, v123, vcc
	v_add_co_u32_e32 v106, vcc, s26, v122
	global_load_dwordx4 v[94:97], v[94:95], off nt
	s_nop 0
	global_load_dwordx4 v[102:105], v[102:103], off nt
	v_addc_co_u32_e32 v107, vcc, 0, v123, vcc
	v_add_co_u32_e32 v108, vcc, s27, v122
	s_nop 1
	v_addc_co_u32_e32 v109, vcc, 0, v123, vcc
	global_load_dwordx4 v[110:113], v[106:107], off nt
	global_load_dwordx4 v[118:121], v[108:109], off nt
	v_add_co_u32_e32 v106, vcc, 0x30000, v122
	s_nop 1
	v_addc_co_u32_e32 v107, vcc, 0, v123, vcc
	v_add_co_u32_e32 v114, vcc, 0x34000, v122
	s_nop 1
	v_addc_co_u32_e32 v115, vcc, 0, v123, vcc
	v_add_co_u32_e32 v124, vcc, 0x38000, v122
	global_load_dwordx4 v[106:109], v[106:107], off nt
	s_nop 0
	global_load_dwordx4 v[114:117], v[114:115], off nt
	v_addc_co_u32_e32 v125, vcc, 0, v123, vcc
	v_add_co_u32_e32 v126, vcc, 0x3c000, v122
	s_nop 1
	v_addc_co_u32_e32 v127, vcc, 0, v123, vcc
	global_load_dwordx4 v[122:125], v[124:125], off nt
	s_nop 0
	global_load_dwordx4 v[126:129], v[126:127], off nt
	s_branch .LBB0_220
.LBB0_227:
	v_readlane_b32 s0, v252, 14
	s_cmpk_gt_i32 s0, 0x1fff
	s_waitcnt vmcnt(62)
	v_lshlrev_b32_e32 v196, 2, v1
	s_cbranch_scc1 .LBB0_236
	s_waitcnt lgkmcnt(0)
	s_add_u32 s10, s82, 0x24000000
	v_readlane_b32 s33, v252, 14
	s_addc_u32 s11, s83, 0
	s_ashr_i32 s0, s33, 31
	s_lshr_b32 s0, s0, 24
	s_add_i32 s2, s33, s0
	s_ashr_i32 s0, s2, 8
	s_ashr_i32 s1, s0, 31
	s_lshl_b64 s[0:1], s[0:1], 24
	s_add_u32 s0, s14, s0
	s_addc_u32 s1, s15, s1
	s_and_b32 s2, s2, 0xffffff00
	s_sub_i32 s2, s33, s2
	s_lshr_b32 s3, s2, 3
	s_bfe_i32 s4, s3, 0x80000
	s_bfe_u32 s4, s4, 0x2000d
	s_add_i32 s4, s3, s4
	s_bfe_i32 s5, s4, 0x80000
	s_and_b32 s4, s4, 0xfc
	s_sub_i32 s3, s3, s4
	s_sext_i32_i8 s3, s3
	s_lshl_b32 s2, s2, 6
	s_lshl_b32 s3, s3, 9
	s_and_b32 s4, s2, 0x100
	s_sext_i32_i16 s5, s5
	s_or_b32 s3, s3, s4
	v_and_b32_e32 v137, 48, v0
	s_waitcnt vmcnt(31)
	v_or_b32_e32 v42, s3, v137
	s_lshl_b32 s3, s5, 6
	s_and_b32 s3, s3, 0xffffff00
	s_and_b32 s2, s2, 0xc0
	v_ashrrev_i32_e32 v43, 31, v42
	s_or_b32 s2, s3, s2
	v_lshlrev_b64 v[2:3], 13, v[42:43]
	s_ashr_i32 s3, s2, 31
	v_lshl_add_u64 v[2:3], s[0:1], 0, v[2:3]
	s_lshl_b64 s[2:3], s[2:3], 2
	v_mov_b32_e32 v197, 0
	v_lshl_add_u64 v[2:3], v[2:3], 0, s[2:3]
	v_lshlrev_b64 v[130:131], 2, v[196:197]
	v_lshl_add_u64 v[44:45], v[2:3], 0, v[130:131]
	s_movk_i32 s16, 0x2000
	v_add_co_u32_e32 v10, vcc, s16, v44
	s_movk_i32 s17, 0x4000
	s_nop 0
	v_addc_co_u32_e32 v11, vcc, 0, v45, vcc
	v_add_co_u32_e32 v14, vcc, s17, v44
	s_movk_i32 s18, 0x6000
	s_nop 0
	v_addc_co_u32_e32 v15, vcc, 0, v45, vcc
	v_add_co_u32_e32 v16, vcc, s18, v44
	s_mov_b32 s19, 0x8000
	s_nop 0
	v_addc_co_u32_e32 v17, vcc, 0, v45, vcc
	v_add_co_u32_e32 v26, vcc, s19, v44
	s_mov_b32 s20, 0xa000
	s_nop 0
	v_addc_co_u32_e32 v27, vcc, 0, v45, vcc
	v_add_co_u32_e32 v28, vcc, s20, v44
	s_mov_b32 s21, 0xc000
	s_nop 0
	v_addc_co_u32_e32 v29, vcc, 0, v45, vcc
	v_add_co_u32_e32 v30, vcc, s21, v44
	s_mov_b32 s22, 0xe000
	s_nop 0
	v_addc_co_u32_e32 v31, vcc, 0, v45, vcc
	v_add_co_u32_e32 v32, vcc, s22, v44
	s_mov_b32 s23, 0x10000
	s_nop 0
	v_addc_co_u32_e32 v33, vcc, 0, v45, vcc
	s_waitcnt vmcnt(30)
	v_add_co_u32_e32 v46, vcc, s23, v44
	s_mov_b32 s24, 0x12000
	s_nop 0
	v_addc_co_u32_e32 v47, vcc, 0, v45, vcc
	v_add_co_u32_e32 v48, vcc, s24, v44
	s_mov_b32 s25, 0x14000
	s_nop 0
	v_addc_co_u32_e32 v49, vcc, 0, v45, vcc
	global_load_dwordx4 v[2:5], v[44:45], off nt
	global_load_dwordx4 v[6:9], v[10:11], off nt
	s_nop 0
	global_load_dwordx4 v[10:13], v[14:15], off nt
	global_load_dwordx4 v[18:21], v[16:17], off nt
	s_nop 0
	global_load_dwordx4 v[14:17], v[26:27], off nt
	global_load_dwordx4 v[22:25], v[28:29], off nt
	s_nop 0
	global_load_dwordx4 v[26:29], v[30:31], off nt
	global_load_dwordx4 v[34:37], v[32:33], off nt
	s_nop 0
	global_load_dwordx4 v[30:33], v[46:47], off nt
	global_load_dwordx4 v[38:41], v[48:49], off nt
	v_add_co_u32_e32 v46, vcc, s25, v44
	s_mov_b32 s26, 0x16000
	s_nop 0
	v_addc_co_u32_e32 v47, vcc, 0, v45, vcc
	v_add_co_u32_e32 v48, vcc, s26, v44
	s_mov_b32 s27, 0x18000
	s_nop 0
	v_addc_co_u32_e32 v49, vcc, 0, v45, vcc
	global_load_dwordx4 v[54:57], v[46:47], off nt
	global_load_dwordx4 v[62:65], v[48:49], off nt
	v_add_co_u32_e32 v46, vcc, s27, v44
	s_mov_b32 s28, 0x1a000
	s_nop 0
	v_addc_co_u32_e32 v47, vcc, 0, v45, vcc
	v_add_co_u32_e32 v48, vcc, s28, v44
	v_or_b32_e32 v42, 64, v42
	s_nop 0
	v_addc_co_u32_e32 v49, vcc, 0, v45, vcc
	s_mov_b32 s29, 0x1c000
	v_ashrrev_i32_e32 v43, 31, v42
	global_load_dwordx4 v[50:53], v[46:47], off nt
	global_load_dwordx4 v[58:61], v[48:49], off nt
	v_add_co_u32_e32 v46, vcc, s29, v44
	v_lshlrev_b64 v[42:43], 13, v[42:43]
	s_nop 0
	v_addc_co_u32_e32 v47, vcc, 0, v45, vcc
	s_mov_b32 s30, 0x1e000
	v_lshl_add_u64 v[42:43], s[0:1], 0, v[42:43]
	v_add_co_u32_e32 v44, vcc, s30, v44
	v_lshl_add_u64 v[42:43], v[42:43], 0, s[2:3]
	s_nop 0
	v_addc_co_u32_e32 v45, vcc, 0, v45, vcc
	s_waitcnt vmcnt(31)
	v_lshl_add_u64 v[122:123], v[42:43], 0, v[130:131]
	s_waitcnt vmcnt(28)
	v_add_co_u32_e32 v66, vcc, s16, v122
	global_load_dwordx4 v[82:85], v[46:47], off nt
	global_load_dwordx4 v[86:89], v[44:45], off nt
	s_waitcnt vmcnt(29)
	v_addc_co_u32_e32 v67, vcc, 0, v123, vcc
	global_load_dwordx4 v[42:45], v[122:123], off nt
	global_load_dwordx4 v[46:49], v[66:67], off nt
	v_add_co_u32_e32 v66, vcc, s17, v122
	v_lshlrev_b32_e32 v132, 4, v1
	s_nop 0
	v_addc_co_u32_e32 v67, vcc, 0, v123, vcc
	s_waitcnt vmcnt(30)
	v_add_co_u32_e32 v68, vcc, s18, v122
	s_movk_i32 s0, 0x410
	s_waitcnt vmcnt(27)
	v_addc_co_u32_e32 v69, vcc, 0, v123, vcc
	v_add_co_u32_e32 v90, vcc, s19, v122
	global_load_dwordx4 v[70:73], v[66:67], off nt
	global_load_dwordx4 v[78:81], v[68:69], off nt
	v_addc_co_u32_e32 v91, vcc, 0, v123, vcc
	v_add_co_u32_e32 v92, vcc, s20, v122
	v_mov_b32_e32 v139, s6
	s_nop 0
	v_addc_co_u32_e32 v93, vcc, 0, v123, vcc
	v_add_co_u32_e32 v94, vcc, s21, v122
	global_load_dwordx4 v[66:69], v[90:91], off nt
	global_load_dwordx4 v[74:77], v[92:93], off nt
	v_addc_co_u32_e32 v95, vcc, 0, v123, vcc
	v_add_co_u32_e32 v96, vcc, s22, v122
	v_add_u32_e32 v134, s6, v137
	s_nop 0
	v_addc_co_u32_e32 v97, vcc, 0, v123, vcc
	v_add_co_u32_e32 v106, vcc, s23, v122
	global_load_dwordx4 v[90:93], v[94:95], off nt
	global_load_dwordx4 v[98:101], v[96:97], off nt
	v_addc_co_u32_e32 v107, vcc, 0, v123, vcc
	v_add_co_u32_e32 v108, vcc, s24, v122
	v_add_u32_e32 v135, s6, v132
	s_nop 0
	v_addc_co_u32_e32 v109, vcc, 0, v123, vcc
	global_load_dwordx4 v[94:97], v[106:107], off nt
	global_load_dwordx4 v[102:105], v[108:109], off nt
	v_add_co_u32_e32 v106, vcc, s25, v122
	v_mul_u32_u24_e32 v154, 0x410, v1
	s_nop 0
	v_addc_co_u32_e32 v107, vcc, 0, v123, vcc
	v_add_co_u32_e32 v108, vcc, s26, v122
	v_mad_u32_u24 v156, v1, s0, v139
	s_nop 0
	v_addc_co_u32_e32 v109, vcc, 0, v123, vcc
	global_load_dwordx4 v[110:113], v[106:107], off nt
	global_load_dwordx4 v[118:121], v[108:109], off nt
	v_add_co_u32_e32 v106, vcc, s27, v122
	v_mul_u32_u24_e32 v155, 0x104, v136
	s_nop 0
	v_addc_co_u32_e32 v107, vcc, 0, v123, vcc
	v_add_co_u32_e32 v114, vcc, s28, v122
	v_or_b32_e32 v138, 64, v137
	s_nop 0
	v_addc_co_u32_e32 v115, vcc, 0, v123, vcc
	v_add_co_u32_e32 v124, vcc, s29, v122
	global_load_dwordx4 v[106:109], v[106:107], off nt
	s_nop 0
	global_load_dwordx4 v[114:117], v[114:115], off nt
	v_addc_co_u32_e32 v125, vcc, 0, v123, vcc
	v_add_co_u32_e32 v126, vcc, s30, v122
	v_mov_b32_e32 v133, v197
	s_nop 0
	v_addc_co_u32_e32 v127, vcc, 0, v123, vcc
	global_load_dwordx4 v[122:125], v[124:125], off nt
	s_nop 0
	global_load_dwordx4 v[126:129], v[126:127], off nt
	v_or_b32_e32 v139, 4, v136
	v_or_b32_e32 v140, 8, v136
	v_or_b32_e32 v141, 12, v136
	v_or_b32_e32 v142, 16, v136
	v_or_b32_e32 v143, 20, v136
	v_or_b32_e32 v144, 24, v136
	v_or_b32_e32 v145, 28, v136
	v_or_b32_e32 v146, 32, v136
	v_or_b32_e32 v147, 36, v136
	v_or_b32_e32 v148, 40, v136
	v_or_b32_e32 v149, 44, v136
	v_or_b32_e32 v150, 48, v136
	v_or_b32_e32 v151, 52, v136
	v_or_b32_e32 v152, 56, v136
	v_or_b32_e32 v153, 60, v136
	s_lshl_b32 s34, s33, 6
	s_lshl_b32 s31, s85, 6
	v_add_u32_e32 v154, v134, v154
	v_add_u32_e32 v155, v135, v155
	v_add_u32_e32 v156, v156, v137
	s_waitcnt vmcnt(0)
	s_branch .LBB0_230

.LBB0_230:
	s_waitcnt vmcnt(47)
	v_mul_f32_e32 v134, 0x42800000, v2
	s_waitcnt vmcnt(46)
	v_mul_f32_e32 v6, 0x42800000, v6
	v_mov_b32_e32 v2, 0
	v_cvt_pk_fp8_f32 v2, v134, v6
	v_mul_f32_e32 v3, 0x42800000, v3
	v_mul_f32_e32 v6, 0x42800000, v7
	v_mov_b32_e32 v7, 0
	v_cvt_pk_fp8_f32 v7, v3, v6
	s_waitcnt vmcnt(45)
	v_mul_f32_e32 v3, 0x42800000, v11
	s_waitcnt vmcnt(44)
	v_mul_f32_e32 v6, 0x42800000, v19
	v_mul_f32_e32 v10, 0x42800000, v10
	v_cvt_pk_fp8_f32 v7, v3, v6 op_sel:[0,0,1]
	v_mul_f32_e32 v3, 0x42800000, v4
	v_mul_f32_e32 v4, 0x42800000, v8
	v_mov_b32_e32 v6, 0
	v_cvt_pk_fp8_f32 v6, v3, v4
	v_mul_f32_e32 v18, 0x42800000, v18
	v_mul_f32_e32 v3, 0x42800000, v5
	v_mul_f32_e32 v4, 0x42800000, v9
	v_mov_b32_e32 v5, 0
	v_cvt_pk_fp8_f32 v2, v10, v18 op_sel:[0,0,1]
	v_mul_f32_e32 v8, 0x42800000, v12
	v_mul_f32_e32 v10, 0x42800000, v20
	v_cvt_pk_fp8_f32 v5, v3, v4
	v_cvt_pk_fp8_f32 v6, v8, v10 op_sel:[0,0,1]
	s_waitcnt vmcnt(43)
	v_mul_f32_e32 v9, 0x42800000, v15
	s_waitcnt vmcnt(42)
	v_mul_f32_e32 v10, 0x42800000, v23
	v_mov_b32_e32 v11, 0
	v_cvt_pk_fp8_f32 v11, v9, v10
	v_mul_f32_e32 v3, 0x42800000, v13
	v_mul_f32_e32 v4, 0x42800000, v21
	v_cvt_pk_fp8_f32 v5, v3, v4 op_sel:[0,0,1]
	v_mul_f32_e32 v4, 0x42800000, v14
	v_mul_f32_e32 v8, 0x42800000, v22
	v_mov_b32_e32 v3, 0
	v_cvt_pk_fp8_f32 v3, v4, v8
	s_waitcnt vmcnt(41)
	v_mul_f32_e32 v4, 0x42800000, v27
	s_waitcnt vmcnt(40)
	v_mul_f32_e32 v8, 0x42800000, v35
	v_cvt_pk_fp8_f32 v11, v4, v8 op_sel:[0,0,1]
	v_mul_f32_e32 v9, 0x42800000, v17
	v_mul_f32_e32 v10, 0x42800000, v25
	v_mul_f32_e32 v4, 0x42800000, v26
	ds_write2_b32 v154, v7, v11 offset0:65 offset1:66
	v_mov_b32_e32 v11, 0
	v_cvt_pk_fp8_f32 v11, v9, v10
	v_mul_f32_e32 v8, 0x42800000, v34
	v_cvt_pk_fp8_f32 v3, v4, v8 op_sel:[0,0,1]
	v_mul_f32_e32 v4, 0x42800000, v16
	v_mul_f32_e32 v8, 0x42800000, v24
	v_mov_b32_e32 v7, 0
	v_cvt_pk_fp8_f32 v7, v4, v8
	v_mul_f32_e32 v4, 0x42800000, v29
	v_mul_f32_e32 v8, 0x42800000, v37
	v_cvt_pk_fp8_f32 v11, v4, v8 op_sel:[0,0,1]
	v_mul_f32_e32 v4, 0x42800000, v28
	v_mul_f32_e32 v8, 0x42800000, v36
	v_cvt_pk_fp8_f32 v7, v4, v8 op_sel:[0,0,1]
	ds_write2_b32 v154, v5, v11 offset0:195 offset1:196
	s_waitcnt vmcnt(39)
	v_mul_f32_e32 v5, 0x42800000, v30
	s_waitcnt vmcnt(38)
	v_mul_f32_e32 v8, 0x42800000, v38
	v_mov_b32_e32 v4, 0
	v_cvt_pk_fp8_f32 v4, v5, v8
	v_mul_f32_e32 v5, 0x42800000, v31
	v_mul_f32_e32 v8, 0x42800000, v39
	v_mov_b32_e32 v11, 0
	v_cvt_pk_fp8_f32 v11, v5, v8
	s_mov_b32 s6, s33
	s_waitcnt vmcnt(37)
	v_mul_f32_e32 v9, 0x42800000, v54
	s_waitcnt vmcnt(36)
	v_mul_f32_e32 v10, 0x42800000, v62
	v_mul_f32_e32 v5, 0x42800000, v55
	v_mul_f32_e32 v8, 0x42800000, v63
	v_cvt_pk_fp8_f32 v4, v9, v10 op_sel:[0,0,1]
	v_cvt_pk_fp8_f32 v11, v5, v8 op_sel:[0,0,1]
	v_mul_f32_e32 v5, 0x42800000, v32
	v_mul_f32_e32 v9, 0x42800000, v40
	v_mov_b32_e32 v8, 0
	s_ashr_i32 s0, s6, 31
	v_cvt_pk_fp8_f32 v8, v5, v9
	v_mul_f32_e32 v5, 0x42800000, v33
	v_mul_f32_e32 v9, 0x42800000, v41
	v_mov_b32_e32 v13, 0
	s_lshr_b32 s0, s0, 24
	v_cvt_pk_fp8_f32 v13, v5, v9
	s_add_i32 s7, s6, s0
	s_ashr_i32 s2, s7, 8
	s_ashr_i32 s3, s2, 31
	s_add_i32 s33, s33, s85
	v_mul_f32_e32 v10, 0x42800000, v56
	v_mul_f32_e32 v12, 0x42800000, v64
	v_mul_f32_e32 v5, 0x42800000, v57
	v_mul_f32_e32 v9, 0x42800000, v65
	s_lshl_b64 s[0:1], s[2:3], 24
	v_cvt_pk_fp8_f32 v8, v10, v12 op_sel:[0,0,1]
	v_cvt_pk_fp8_f32 v13, v5, v9 op_sel:[0,0,1]
	s_waitcnt vmcnt(35)
	v_mul_f32_e32 v9, 0x42800000, v50
	s_waitcnt vmcnt(34)
	v_mul_f32_e32 v10, 0x42800000, v58
	v_mov_b32_e32 v5, 0
	s_add_u32 s4, s14, s0
	v_cvt_pk_fp8_f32 v5, v9, v10
	v_mul_f32_e32 v9, 0x42800000, v51
	v_mul_f32_e32 v10, 0x42800000, v59
	v_mov_b32_e32 v15, 0
	s_addc_u32 s5, s15, s1
	s_and_b32 s0, s7, 0x7ff00
	v_cvt_pk_fp8_f32 v15, v9, v10
	s_sub_i32 s0, s6, s0
	s_lshr_b32 s0, s0, 3
	s_bfe_i32 s1, s0, 0x80000
	s_waitcnt vmcnt(33)
	v_mul_f32_e32 v12, 0x42800000, v82
	s_waitcnt vmcnt(32)
	v_mul_f32_e32 v14, 0x42800000, v86
	v_mul_f32_e32 v9, 0x42800000, v83
	v_mul_f32_e32 v10, 0x42800000, v87
	s_bfe_u32 s1, s1, 0x2000d
	v_cvt_pk_fp8_f32 v5, v12, v14 op_sel:[0,0,1]
	v_cvt_pk_fp8_f32 v15, v9, v10 op_sel:[0,0,1]
	v_mul_f32_e32 v10, 0x42800000, v52
	v_mul_f32_e32 v12, 0x42800000, v60
	v_mov_b32_e32 v9, 0
	s_add_i32 s1, s0, s1
	v_cvt_pk_fp8_f32 v9, v10, v12
	v_mul_f32_e32 v10, 0x42800000, v53
	v_mul_f32_e32 v12, 0x42800000, v61
	v_mov_b32_e32 v17, 0
	s_bfe_i32 s6, s1, 0x80000
	s_and_b32 s1, s1, 0xfc
	v_cvt_pk_fp8_f32 v17, v10, v12
	s_sub_i32 s0, s0, s1
	s_lshl_b32 s1, s2, 14
	s_sext_i32_i8 s0, s0
	s_sub_i32 s1, s34, s1
	v_mul_f32_e32 v14, 0x42800000, v84
	v_mul_f32_e32 v16, 0x42800000, v88
	s_lshl_b32 s0, s0, 9
	s_and_b32 s7, s1, 0x100
	v_cvt_pk_fp8_f32 v9, v14, v16 op_sel:[0,0,1]
	v_mul_f32_e32 v10, 0x42800000, v85
	v_mul_f32_e32 v12, 0x42800000, v89
	s_sext_i32_i16 s6, s6
	s_or_b32 s35, s0, s7
	v_cvt_pk_fp8_f32 v17, v10, v12 op_sel:[0,0,1]
	v_or_b32_e32 v134, s35, v137
	s_lshl_b32 s0, s6, 6
	ds_write_b128 v154, v[2:5]
	ds_write2_b32 v154, v11, v15 offset0:67 offset1:68
	ds_write2_b64 v154, v[6:7], v[8:9] offset0:65 offset1:66
	ds_write2_b32 v154, v13, v17 offset0:197 offset1:198
	v_or_b32_e32 v2, 0x80, v134
	s_and_b32 s0, s0, 0xffffff00
	s_and_b32 s1, s1, 0xc0
	v_ashrrev_i32_e32 v3, 31, v2
	s_or_b32 s0, s0, s1
	v_lshlrev_b64 v[2:3], 13, v[2:3]
	s_ashr_i32 s1, s0, 31
	v_lshl_add_u64 v[2:3], s[4:5], 0, v[2:3]
	s_lshl_b64 s[6:7], s[0:1], 2
	v_lshl_add_u64 v[2:3], v[2:3], 0, s[6:7]
	v_lshl_add_u64 v[82:83], v[2:3], 0, v[130:131]
	v_add_co_u32_e32 v6, vcc, s16, v82
	s_waitcnt vmcnt(31)
	v_mul_f32_e32 v135, 0x42800000, v42
	v_addc_co_u32_e32 v7, vcc, 0, v83, vcc
	v_add_co_u32_e32 v10, vcc, s17, v82
	global_load_dwordx4 v[2:5], v[82:83], off nt
	s_nop 0
	global_load_dwordx4 v[6:9], v[6:7], off nt
	v_addc_co_u32_e32 v11, vcc, 0, v83, vcc
	v_add_co_u32_e32 v14, vcc, s18, v82
	s_waitcnt vmcnt(32)
	v_mul_f32_e32 v46, 0x42800000, v46
	v_addc_co_u32_e32 v15, vcc, 0, v83, vcc
	global_load_dwordx4 v[10:13], v[10:11], off nt
	s_nop 0
	global_load_dwordx4 v[18:21], v[14:15], off nt
	v_add_co_u32_e32 v14, vcc, s19, v82
	v_mov_b32_e32 v42, 0
	s_nop 0
	v_addc_co_u32_e32 v15, vcc, 0, v83, vcc
	v_add_co_u32_e32 v22, vcc, s20, v82
	v_cvt_pk_fp8_f32 v42, v135, v46
	s_nop 0
	v_addc_co_u32_e32 v23, vcc, 0, v83, vcc
	v_add_co_u32_e32 v26, vcc, s21, v82
	v_mul_f32_e32 v43, 0x42800000, v43
	v_mul_f32_e32 v46, 0x42800000, v47
	v_mov_b32_e32 v47, 0
	v_addc_co_u32_e32 v27, vcc, 0, v83, vcc
	v_cvt_pk_fp8_f32 v47, v43, v46
	v_add_co_u32_e32 v30, vcc, s22, v82
	global_load_dwordx4 v[14:17], v[14:15], off nt
	s_nop 0
	global_load_dwordx4 v[22:25], v[22:23], off nt
	v_addc_co_u32_e32 v31, vcc, 0, v83, vcc
	global_load_dwordx4 v[26:29], v[26:27], off nt
	s_nop 0
	global_load_dwordx4 v[34:37], v[30:31], off nt
	v_add_co_u32_e32 v30, vcc, s23, v82
	s_waitcnt vmcnt(37)
	v_mul_f32_e32 v43, 0x42800000, v71
	s_waitcnt vmcnt(36)
	v_mul_f32_e32 v46, 0x42800000, v79
	v_addc_co_u32_e32 v31, vcc, 0, v83, vcc
	v_cvt_pk_fp8_f32 v47, v43, v46 op_sel:[0,0,1]
	v_mul_f32_e32 v43, 0x42800000, v44
	v_mul_f32_e32 v44, 0x42800000, v48
	v_mov_b32_e32 v46, 0
	v_add_co_u32_e32 v38, vcc, s24, v82
	v_cvt_pk_fp8_f32 v46, v43, v44
	v_mul_f32_e32 v43, 0x42800000, v45
	v_mul_f32_e32 v44, 0x42800000, v49
	v_mov_b32_e32 v45, 0
	v_addc_co_u32_e32 v39, vcc, 0, v83, vcc
	v_cvt_pk_fp8_f32 v45, v43, v44
	v_add_co_u32_e32 v50, vcc, s25, v82
	v_mul_f32_e32 v43, 0x42800000, v73
	s_nop 0
	v_addc_co_u32_e32 v51, vcc, 0, v83, vcc
	v_add_co_u32_e32 v52, vcc, s26, v82
	v_mul_f32_e32 v44, 0x42800000, v81
	s_nop 0
	v_addc_co_u32_e32 v53, vcc, 0, v83, vcc
	v_cvt_pk_fp8_f32 v45, v43, v44 op_sel:[0,0,1]
	s_waitcnt vmcnt(35)
	v_mul_f32_e32 v44, 0x42800000, v66
	v_mul_f32_e32 v49, 0x42800000, v67
	s_waitcnt vmcnt(34)
	v_mul_f32_e32 v66, 0x42800000, v75
	v_mov_b32_e32 v67, 0
	global_load_dwordx4 v[30:33], v[30:31], off nt
	s_nop 0
	global_load_dwordx4 v[38:41], v[38:39], off nt
	s_nop 0
	global_load_dwordx4 v[54:57], v[50:51], off nt
	global_load_dwordx4 v[62:65], v[52:53], off nt
	v_add_co_u32_e32 v50, vcc, s27, v82
	v_mul_f32_e32 v70, 0x42800000, v70
	v_mul_f32_e32 v78, 0x42800000, v78
	v_cvt_pk_fp8_f32 v67, v49, v66
	v_addc_co_u32_e32 v51, vcc, 0, v83, vcc
	v_cvt_pk_fp8_f32 v42, v70, v78 op_sel:[0,0,1]
	v_mul_f32_e32 v48, 0x42800000, v72
	v_mul_f32_e32 v70, 0x42800000, v80
	v_add_co_u32_e32 v58, vcc, s28, v82
	v_cvt_pk_fp8_f32 v46, v48, v70 op_sel:[0,0,1]
	v_mul_f32_e32 v48, 0x42800000, v74
	v_mov_b32_e32 v43, 0
	v_addc_co_u32_e32 v59, vcc, 0, v83, vcc
	v_cvt_pk_fp8_f32 v43, v44, v48
	s_waitcnt vmcnt(37)
	v_mul_f32_e32 v44, 0x42800000, v91
	s_waitcnt vmcnt(36)
	v_mul_f32_e32 v48, 0x42800000, v99
	v_add_co_u32_e32 v84, vcc, s29, v82
	v_cvt_pk_fp8_f32 v67, v44, v48 op_sel:[0,0,1]
	s_nop 0
	v_addc_co_u32_e32 v85, vcc, 0, v83, vcc
	v_add_co_u32_e32 v86, vcc, s30, v82
	global_load_dwordx4 v[50:53], v[50:51], off nt
	s_nop 0
	global_load_dwordx4 v[58:61], v[58:59], off nt
	v_addc_co_u32_e32 v87, vcc, 0, v83, vcc
	global_load_dwordx4 v[82:85], v[84:85], off nt
	s_nop 0
	global_load_dwordx4 v[86:89], v[86:87], off nt
	ds_write2_b32 v156, v47, v67 offset0:81 offset1:82
	v_mul_f32_e32 v49, 0x42800000, v69
	v_mul_f32_e32 v66, 0x42800000, v77
	v_mov_b32_e32 v67, 0
	v_cvt_pk_fp8_f32 v67, v49, v66
	v_mul_f32_e32 v44, 0x42800000, v90
	v_mul_f32_e32 v48, 0x42800000, v98
	v_cvt_pk_fp8_f32 v43, v44, v48 op_sel:[0,0,1]
	v_mul_f32_e32 v44, 0x42800000, v68
	v_mul_f32_e32 v48, 0x42800000, v76
	v_mov_b32_e32 v47, 0
	v_cvt_pk_fp8_f32 v47, v44, v48
	v_mul_f32_e32 v44, 0x42800000, v93
	v_mul_f32_e32 v48, 0x42800000, v101
	v_cvt_pk_fp8_f32 v67, v44, v48 op_sel:[0,0,1]
	v_mul_f32_e32 v44, 0x42800000, v92
	v_mul_f32_e32 v48, 0x42800000, v100
	v_cvt_pk_fp8_f32 v47, v44, v48 op_sel:[0,0,1]
	ds_write2_b32 v156, v45, v67 offset0:211 offset1:212
	s_waitcnt vmcnt(39)
	v_mul_f32_e32 v45, 0x42800000, v94
	s_waitcnt vmcnt(38)
	v_mul_f32_e32 v48, 0x42800000, v102
	v_mov_b32_e32 v44, 0
	v_cvt_pk_fp8_f32 v44, v45, v48
	v_mul_f32_e32 v45, 0x42800000, v95
	v_mul_f32_e32 v48, 0x42800000, v103
	v_mov_b32_e32 v67, 0
	v_cvt_pk_fp8_f32 v67, v45, v48
	s_waitcnt vmcnt(37)
	v_mul_f32_e32 v49, 0x42800000, v110
	s_waitcnt vmcnt(36)
	v_mul_f32_e32 v66, 0x42800000, v118
	v_mul_f32_e32 v45, 0x42800000, v111
	v_mul_f32_e32 v48, 0x42800000, v119
	v_cvt_pk_fp8_f32 v44, v49, v66 op_sel:[0,0,1]
	v_cvt_pk_fp8_f32 v67, v45, v48 op_sel:[0,0,1]
	v_mul_f32_e32 v45, 0x42800000, v96
	v_mul_f32_e32 v49, 0x42800000, v104
	v_mov_b32_e32 v48, 0
	v_cvt_pk_fp8_f32 v48, v45, v49
	v_mul_f32_e32 v45, 0x42800000, v97
	v_mul_f32_e32 v49, 0x42800000, v105
	v_mov_b32_e32 v69, 0
	v_cvt_pk_fp8_f32 v69, v45, v49
	v_mul_f32_e32 v66, 0x42800000, v112
	v_mul_f32_e32 v68, 0x42800000, v120
	v_mul_f32_e32 v45, 0x42800000, v113
	v_mul_f32_e32 v49, 0x42800000, v121
	v_cvt_pk_fp8_f32 v48, v66, v68 op_sel:[0,0,1]
	v_cvt_pk_fp8_f32 v69, v45, v49 op_sel:[0,0,1]
	s_waitcnt vmcnt(35)
	v_mul_f32_e32 v49, 0x42800000, v106
	s_waitcnt vmcnt(34)
	v_mul_f32_e32 v66, 0x42800000, v114
	v_mov_b32_e32 v45, 0
	v_cvt_pk_fp8_f32 v45, v49, v66
	v_mul_f32_e32 v49, 0x42800000, v107
	v_mul_f32_e32 v66, 0x42800000, v115
	v_mov_b32_e32 v71, 0
	v_cvt_pk_fp8_f32 v71, v49, v66
	s_waitcnt vmcnt(33)
	v_mul_f32_e32 v68, 0x42800000, v122
	s_waitcnt vmcnt(32)
	v_mul_f32_e32 v70, 0x42800000, v126
	v_mul_f32_e32 v49, 0x42800000, v123
	v_mul_f32_e32 v66, 0x42800000, v127
	v_cvt_pk_fp8_f32 v45, v68, v70 op_sel:[0,0,1]
	v_cvt_pk_fp8_f32 v71, v49, v66 op_sel:[0,0,1]
	v_mul_f32_e32 v66, 0x42800000, v108
	v_mul_f32_e32 v68, 0x42800000, v116
	v_mov_b32_e32 v49, 0
	v_cvt_pk_fp8_f32 v49, v66, v68
	v_mul_f32_e32 v66, 0x42800000, v109
	v_mul_f32_e32 v68, 0x42800000, v117
	v_mov_b32_e32 v73, 0
	v_cvt_pk_fp8_f32 v73, v66, v68
	v_mul_f32_e32 v70, 0x42800000, v124
	v_mul_f32_e32 v72, 0x42800000, v128
	v_cvt_pk_fp8_f32 v49, v70, v72 op_sel:[0,0,1]
	v_mul_f32_e32 v66, 0x42800000, v125
	v_mul_f32_e32 v68, 0x42800000, v129
	v_cvt_pk_fp8_f32 v73, v66, v68 op_sel:[0,0,1]
	ds_write_b128 v156, v[42:45] offset:64
	ds_write2_b32 v156, v67, v71 offset0:83 offset1:84
	ds_write2_b64 v156, v[46:47], v[48:49] offset0:73 offset1:74
	ds_write2_b32 v156, v69, v73 offset0:213 offset1:214
	v_or_b32_e32 v42, 0xc0, v134
	v_ashrrev_i32_e32 v43, 31, v42
	v_lshlrev_b64 v[42:43], 13, v[42:43]
	v_lshl_add_u64 v[42:43], s[4:5], 0, v[42:43]
	v_lshl_add_u64 v[42:43], v[42:43], 0, s[6:7]
	v_lshl_add_u64 v[122:123], v[42:43], 0, v[130:131]
	v_add_co_u32_e32 v46, vcc, s16, v122
	s_waitcnt vmcnt(15)
	v_mul_f32_e32 v134, 0x42800000, v2
	v_addc_co_u32_e32 v47, vcc, 0, v123, vcc
	v_add_co_u32_e32 v66, vcc, s17, v122
	global_load_dwordx4 v[42:45], v[122:123], off nt
	s_nop 0
	global_load_dwordx4 v[46:49], v[46:47], off nt
	v_addc_co_u32_e32 v67, vcc, 0, v123, vcc
	v_add_co_u32_e32 v68, vcc, s18, v122
	s_waitcnt vmcnt(16)
	v_mul_f32_e32 v135, 0x42800000, v6
	v_addc_co_u32_e32 v69, vcc, 0, v123, vcc
	global_load_dwordx4 v[70:73], v[66:67], off nt
	global_load_dwordx4 v[78:81], v[68:69], off nt
	v_add_co_u32_e32 v66, vcc, s19, v122
	v_mov_b32_e32 v158, 0
	s_nop 0
	v_addc_co_u32_e32 v67, vcc, 0, v123, vcc
	v_add_co_u32_e32 v74, vcc, s20, v122
	v_cvt_pk_fp8_f32 v158, v134, v135
	s_nop 0
	v_addc_co_u32_e32 v75, vcc, 0, v123, vcc
	v_add_co_u32_e32 v90, vcc, s21, v122
	global_load_dwordx4 v[66:69], v[66:67], off nt
	s_nop 0
	global_load_dwordx4 v[74:77], v[74:75], off nt
	v_addc_co_u32_e32 v91, vcc, 0, v123, vcc
	v_add_co_u32_e32 v94, vcc, s22, v122
	v_mul_f32_e32 v134, 0x42800000, v3
	s_nop 0
	v_addc_co_u32_e32 v95, vcc, 0, v123, vcc
	global_load_dwordx4 v[90:93], v[90:91], off nt
	s_nop 0
	global_load_dwordx4 v[98:101], v[94:95], off nt
	v_add_co_u32_e32 v94, vcc, s23, v122
	v_mul_f32_e32 v135, 0x42800000, v7
	s_nop 0
	v_addc_co_u32_e32 v95, vcc, 0, v123, vcc
	v_add_co_u32_e32 v102, vcc, s24, v122
	v_mov_b32_e32 v160, 0
	s_nop 0
	v_addc_co_u32_e32 v103, vcc, 0, v123, vcc
	v_add_co_u32_e32 v106, vcc, s25, v122
	global_load_dwordx4 v[94:97], v[94:95], off nt
	s_nop 0
	global_load_dwordx4 v[102:105], v[102:103], off nt
	v_addc_co_u32_e32 v107, vcc, 0, v123, vcc
	v_add_co_u32_e32 v108, vcc, s26, v122
	v_cvt_pk_fp8_f32 v160, v134, v135
	s_nop 0
	v_addc_co_u32_e32 v109, vcc, 0, v123, vcc
	global_load_dwordx4 v[110:113], v[106:107], off nt
	global_load_dwordx4 v[118:121], v[108:109], off nt
	v_add_co_u32_e32 v106, vcc, s27, v122
	s_waitcnt vmcnt(25)
	v_mul_f32_e32 v157, 0x42800000, v10
	v_addc_co_u32_e32 v107, vcc, 0, v123, vcc
	v_add_co_u32_e32 v114, vcc, s28, v122
	s_waitcnt vmcnt(24)
	v_mul_f32_e32 v159, 0x42800000, v18
	v_addc_co_u32_e32 v115, vcc, 0, v123, vcc
	v_add_co_u32_e32 v124, vcc, s29, v122
	global_load_dwordx4 v[106:109], v[106:107], off nt
	s_nop 0
	global_load_dwordx4 v[114:117], v[114:115], off nt
	v_addc_co_u32_e32 v125, vcc, 0, v123, vcc
	v_add_co_u32_e32 v126, vcc, s30, v122
	v_mul_f32_e32 v134, 0x42800000, v11
	s_nop 0
	v_addc_co_u32_e32 v127, vcc, 0, v123, vcc
	global_load_dwordx4 v[122:125], v[124:125], off nt
	s_nop 0
	global_load_dwordx4 v[126:129], v[126:127], off nt
	v_mul_f32_e32 v135, 0x42800000, v19
	v_cvt_pk_fp8_f32 v158, v157, v159 op_sel:[0,0,1]
	v_cvt_pk_fp8_f32 v160, v134, v135 op_sel:[0,0,1]
	v_mul_f32_e32 v135, 0x42800000, v4
	v_mul_f32_e32 v157, 0x42800000, v8
	v_mov_b32_e32 v134, 0
	v_cvt_pk_fp8_f32 v134, v135, v157
	v_mul_f32_e32 v135, 0x42800000, v5
	v_mul_f32_e32 v157, 0x42800000, v9
	v_mov_b32_e32 v162, 0
	v_mul_f32_e32 v159, 0x42800000, v12
	v_mul_f32_e32 v161, 0x42800000, v20
	v_cvt_pk_fp8_f32 v162, v135, v157
	v_cvt_pk_fp8_f32 v134, v159, v161 op_sel:[0,0,1]
	s_waitcnt vmcnt(27)
	v_mul_f32_e32 v161, 0x42800000, v15
	s_waitcnt vmcnt(26)
	v_mul_f32_e32 v163, 0x42800000, v23
	v_mov_b32_e32 v164, 0
	v_cvt_pk_fp8_f32 v164, v161, v163
	v_mul_f32_e32 v135, 0x42800000, v13
	v_mul_f32_e32 v157, 0x42800000, v21
	v_cvt_pk_fp8_f32 v162, v135, v157 op_sel:[0,0,1]
	v_mul_f32_e32 v135, 0x42800000, v14
	v_mul_f32_e32 v157, 0x42800000, v22
	v_mov_b32_e32 v159, 0
	v_cvt_pk_fp8_f32 v159, v135, v157
	s_waitcnt vmcnt(25)
	v_mul_f32_e32 v135, 0x42800000, v27
	s_waitcnt vmcnt(24)
	v_mul_f32_e32 v157, 0x42800000, v35
	v_cvt_pk_fp8_f32 v164, v135, v157 op_sel:[0,0,1]
	v_mul_f32_e32 v161, 0x42800000, v17
	v_mul_f32_e32 v163, 0x42800000, v25
	v_mul_f32_e32 v135, 0x42800000, v26
	ds_write2_b32 v156, v160, v164 offset0:97 offset1:98
	v_mov_b32_e32 v164, 0
	v_cvt_pk_fp8_f32 v164, v161, v163
	v_mul_f32_e32 v157, 0x42800000, v34
	v_cvt_pk_fp8_f32 v159, v135, v157 op_sel:[0,0,1]
	v_mul_f32_e32 v157, 0x42800000, v16
	v_mul_f32_e32 v160, 0x42800000, v24
	v_mov_b32_e32 v135, 0
	v_cvt_pk_fp8_f32 v135, v157, v160
	v_mul_f32_e32 v157, 0x42800000, v29
	v_mul_f32_e32 v160, 0x42800000, v37
	v_cvt_pk_fp8_f32 v164, v157, v160 op_sel:[0,0,1]
	v_mul_f32_e32 v157, 0x42800000, v28
	v_mul_f32_e32 v160, 0x42800000, v36
	v_cvt_pk_fp8_f32 v135, v157, v160 op_sel:[0,0,1]
	s_waitcnt vmcnt(23)
	v_mul_f32_e32 v157, 0x42800000, v30
	s_waitcnt vmcnt(22)
	v_mul_f32_e32 v161, 0x42800000, v38
	v_mov_b32_e32 v160, 0
	ds_write2_b32 v156, v162, v164 offset0:227 offset1:228
	v_cvt_pk_fp8_f32 v160, v157, v161
	v_mul_f32_e32 v157, 0x42800000, v31
	v_mul_f32_e32 v161, 0x42800000, v39
	v_mov_b32_e32 v164, 0
	v_cvt_pk_fp8_f32 v164, v157, v161
	s_waitcnt vmcnt(21)
	v_mul_f32_e32 v162, 0x42800000, v54
	s_waitcnt vmcnt(20)
	v_mul_f32_e32 v163, 0x42800000, v62
	v_mul_f32_e32 v157, 0x42800000, v55
	v_mul_f32_e32 v161, 0x42800000, v63
	v_cvt_pk_fp8_f32 v160, v162, v163 op_sel:[0,0,1]
	v_cvt_pk_fp8_f32 v164, v157, v161 op_sel:[0,0,1]
	v_mul_f32_e32 v157, 0x42800000, v32
	v_mul_f32_e32 v161, 0x42800000, v40
	v_mov_b32_e32 v162, 0
	v_cvt_pk_fp8_f32 v162, v157, v161
	v_mul_f32_e32 v157, 0x42800000, v33
	v_mul_f32_e32 v161, 0x42800000, v41
	v_mov_b32_e32 v166, 0
	v_cvt_pk_fp8_f32 v166, v157, v161
	v_mul_f32_e32 v163, 0x42800000, v56
	v_mul_f32_e32 v165, 0x42800000, v64
	v_mul_f32_e32 v157, 0x42800000, v57
	v_mul_f32_e32 v161, 0x42800000, v65
	v_cvt_pk_fp8_f32 v162, v163, v165 op_sel:[0,0,1]
	v_cvt_pk_fp8_f32 v166, v157, v161 op_sel:[0,0,1]
	s_waitcnt vmcnt(19)
	v_mul_f32_e32 v157, 0x42800000, v50
	s_waitcnt vmcnt(18)
	v_mul_f32_e32 v163, 0x42800000, v58
	v_mov_b32_e32 v161, 0
	v_cvt_pk_fp8_f32 v161, v157, v163
	v_mul_f32_e32 v157, 0x42800000, v51
	v_mul_f32_e32 v163, 0x42800000, v59
	v_mov_b32_e32 v168, 0
	v_cvt_pk_fp8_f32 v168, v157, v163
	s_waitcnt vmcnt(17)
	v_mul_f32_e32 v165, 0x42800000, v82
	s_waitcnt vmcnt(16)
	v_mul_f32_e32 v167, 0x42800000, v86
	v_mul_f32_e32 v157, 0x42800000, v83
	v_mul_f32_e32 v163, 0x42800000, v87
	v_cvt_pk_fp8_f32 v161, v165, v167 op_sel:[0,0,1]
	v_cvt_pk_fp8_f32 v168, v157, v163 op_sel:[0,0,1]
	v_mul_f32_e32 v157, 0x42800000, v52
	v_mul_f32_e32 v165, 0x42800000, v60
	v_mov_b32_e32 v163, 0
	v_cvt_pk_fp8_f32 v163, v157, v165
	v_mul_f32_e32 v157, 0x42800000, v53
	v_mul_f32_e32 v165, 0x42800000, v61
	v_mov_b32_e32 v170, 0
	v_cvt_pk_fp8_f32 v170, v157, v165
	v_mul_f32_e32 v167, 0x42800000, v84
	v_mul_f32_e32 v169, 0x42800000, v88
	s_cmpk_gt_i32 s33, 0x1fff
	v_cvt_pk_fp8_f32 v163, v167, v169 op_sel:[0,0,1]
	v_mul_f32_e32 v157, 0x42800000, v85
	v_mul_f32_e32 v165, 0x42800000, v89
	s_cselect_b64 s[4:5], -1, 0
	v_cvt_pk_fp8_f32 v170, v157, v165 op_sel:[0,0,1]
	s_and_b64 vcc, exec, s[4:5]
	ds_write_b128 v156, v[158:161] offset:128
	ds_write2_b32 v156, v164, v168 offset0:99 offset1:100
	ds_write2_b64 v156, v[134:135], v[162:163] offset0:81 offset1:82
	ds_write2_b32 v156, v166, v170 offset0:229 offset1:230
	s_cbranch_vccz .Lcv2_a
	s_waitcnt vmcnt(0)
	s_branch .LBB0_232
.Lcv2_a:
	s_ashr_i32 s1, s33, 31
	s_lshr_b32 s1, s1, 24
	s_add_i32 s1, s33, s1
	s_ashr_i32 s6, s1, 8
	s_ashr_i32 s7, s6, 31
	s_lshl_b64 s[6:7], s[6:7], 24
	s_add_u32 s6, s14, s6
	s_addc_u32 s7, s15, s7
	s_and_b32 s1, s1, 0xffffff00
	s_sub_i32 s1, s33, s1
	s_lshr_b32 s8, s1, 3
	s_bfe_i32 s9, s8, 0x80000
	s_bfe_u32 s9, s9, 0x2000d
	s_add_i32 s9, s8, s9
	s_bfe_i32 s36, s9, 0x80000
	s_and_b32 s9, s9, 0xfc
	s_sub_i32 s8, s8, s9
	s_sext_i32_i8 s8, s8
	s_lshl_b32 s1, s1, 6
	s_lshl_b32 s8, s8, 9
	s_and_b32 s9, s1, 0x100
	s_or_b32 s8, s8, s9
	v_or_b32_e32 v2, s8, v137
	v_ashrrev_i32_e32 v3, 31, v2
	s_sext_i32_i16 s36, s36
	v_lshlrev_b64 v[2:3], 13, v[2:3]
	v_lshl_add_u64 v[2:3], s[6:7], 0, v[2:3]
	s_lshl_b32 s6, s36, 6
	s_and_b32 s6, s6, 0xffffff00
	s_and_b32 s1, s1, 0xc0
	s_or_b32 s6, s6, s1
	s_ashr_i32 s7, s6, 31
	v_lshl_add_u64 v[2:3], s[6:7], 2, v[2:3]
	v_lshl_add_u64 v[82:83], v[196:197], 2, v[2:3]
	v_add_co_u32_e32 v6, vcc, s16, v82
	s_nop 1
	v_addc_co_u32_e32 v7, vcc, 0, v83, vcc
	v_add_co_u32_e32 v10, vcc, s17, v82
	global_load_dwordx4 v[2:5], v[82:83], off nt
	s_nop 0
	global_load_dwordx4 v[6:9], v[6:7], off nt
	v_addc_co_u32_e32 v11, vcc, 0, v83, vcc
	v_add_co_u32_e32 v14, vcc, s18, v82
	s_nop 1
	v_addc_co_u32_e32 v15, vcc, 0, v83, vcc
	global_load_dwordx4 v[10:13], v[10:11], off nt
	s_nop 0
	global_load_dwordx4 v[18:21], v[14:15], off nt
	v_add_co_u32_e32 v14, vcc, s19, v82
	s_nop 1
	v_addc_co_u32_e32 v15, vcc, 0, v83, vcc
	v_add_co_u32_e32 v22, vcc, s20, v82
	s_nop 1
	v_addc_co_u32_e32 v23, vcc, 0, v83, vcc
	v_add_co_u32_e32 v26, vcc, s21, v82
	global_load_dwordx4 v[14:17], v[14:15], off nt
	s_nop 0
	global_load_dwordx4 v[22:25], v[22:23], off nt
	v_addc_co_u32_e32 v27, vcc, 0, v83, vcc
	v_add_co_u32_e32 v30, vcc, s22, v82
	s_nop 1
	v_addc_co_u32_e32 v31, vcc, 0, v83, vcc
	global_load_dwordx4 v[26:29], v[26:27], off nt
	s_nop 0
	global_load_dwordx4 v[34:37], v[30:31], off nt
	v_add_co_u32_e32 v30, vcc, s23, v82
	s_nop 1
	v_addc_co_u32_e32 v31, vcc, 0, v83, vcc
	v_add_co_u32_e32 v38, vcc, s24, v82
	s_nop 1
	v_addc_co_u32_e32 v39, vcc, 0, v83, vcc
	v_add_co_u32_e32 v50, vcc, s25, v82
	global_load_dwordx4 v[30:33], v[30:31], off nt
	s_nop 0
	global_load_dwordx4 v[38:41], v[38:39], off nt
	v_addc_co_u32_e32 v51, vcc, 0, v83, vcc
	v_add_co_u32_e32 v52, vcc, s26, v82
	s_nop 1
	v_addc_co_u32_e32 v53, vcc, 0, v83, vcc
	global_load_dwordx4 v[54:57], v[50:51], off nt
	global_load_dwordx4 v[62:65], v[52:53], off nt
	v_add_co_u32_e32 v50, vcc, 0x18000, v82
	s_nop 1
	v_addc_co_u32_e32 v51, vcc, 0, v83, vcc
	v_add_co_u32_e32 v58, vcc, 0x1a000, v82
	s_nop 1
	v_addc_co_u32_e32 v59, vcc, 0, v83, vcc
	v_add_co_u32_e32 v84, vcc, 0x1c000, v82
	global_load_dwordx4 v[50:53], v[50:51], off nt
	s_nop 0
	global_load_dwordx4 v[58:61], v[58:59], off nt
	v_addc_co_u32_e32 v85, vcc, 0, v83, vcc
	v_add_co_u32_e32 v86, vcc, 0x1e000, v82
	s_nop 1
	v_addc_co_u32_e32 v87, vcc, 0, v83, vcc
	global_load_dwordx4 v[82:85], v[84:85], off nt
	s_nop 0
	global_load_dwordx4 v[86:89], v[86:87], off nt
.LBB0_232:
	s_waitcnt vmcnt(31)
	v_mul_f32_e32 v134, 0x42800000, v42
	s_waitcnt vmcnt(30)
	v_mul_f32_e32 v135, 0x42800000, v46
	v_mov_b32_e32 v158, 0
	v_cvt_pk_fp8_f32 v158, v134, v135
	v_mul_f32_e32 v134, 0x42800000, v43
	v_mul_f32_e32 v135, 0x42800000, v47
	v_mov_b32_e32 v160, 0
	v_cvt_pk_fp8_f32 v160, v134, v135
	s_waitcnt vmcnt(29)
	v_mul_f32_e32 v157, 0x42800000, v70
	s_waitcnt vmcnt(28)
	v_mul_f32_e32 v159, 0x42800000, v78
	v_mul_f32_e32 v134, 0x42800000, v71
	v_mul_f32_e32 v135, 0x42800000, v79
	v_cvt_pk_fp8_f32 v158, v157, v159 op_sel:[0,0,1]
	v_cvt_pk_fp8_f32 v160, v134, v135 op_sel:[0,0,1]
	v_mul_f32_e32 v135, 0x42800000, v44
	v_mul_f32_e32 v157, 0x42800000, v48
	v_mov_b32_e32 v134, 0
	v_cvt_pk_fp8_f32 v134, v135, v157
	v_mul_f32_e32 v135, 0x42800000, v45
	v_mul_f32_e32 v157, 0x42800000, v49
	v_mov_b32_e32 v162, 0
	v_mul_f32_e32 v159, 0x42800000, v72
	v_mul_f32_e32 v161, 0x42800000, v80
	v_cvt_pk_fp8_f32 v162, v135, v157
	v_cvt_pk_fp8_f32 v134, v159, v161 op_sel:[0,0,1]
	s_waitcnt vmcnt(27)
	v_mul_f32_e32 v161, 0x42800000, v67
	s_waitcnt vmcnt(26)
	v_mul_f32_e32 v163, 0x42800000, v75
	v_mov_b32_e32 v164, 0
	v_cvt_pk_fp8_f32 v164, v161, v163
	v_mul_f32_e32 v135, 0x42800000, v73
	v_mul_f32_e32 v157, 0x42800000, v81
	v_cvt_pk_fp8_f32 v162, v135, v157 op_sel:[0,0,1]
	v_mul_f32_e32 v135, 0x42800000, v66
	v_mul_f32_e32 v157, 0x42800000, v74
	v_mov_b32_e32 v159, 0
	v_cvt_pk_fp8_f32 v159, v135, v157
	s_waitcnt vmcnt(25)
	v_mul_f32_e32 v135, 0x42800000, v91
	s_waitcnt vmcnt(24)
	v_mul_f32_e32 v157, 0x42800000, v99
	v_cvt_pk_fp8_f32 v164, v135, v157 op_sel:[0,0,1]
	v_mul_f32_e32 v161, 0x42800000, v69
	v_mul_f32_e32 v163, 0x42800000, v77
	v_mul_f32_e32 v135, 0x42800000, v90
	ds_write2_b32 v156, v160, v164 offset0:113 offset1:114
	v_mov_b32_e32 v164, 0
	v_cvt_pk_fp8_f32 v164, v161, v163
	v_mul_f32_e32 v157, 0x42800000, v98
	v_cvt_pk_fp8_f32 v159, v135, v157 op_sel:[0,0,1]
	v_mul_f32_e32 v157, 0x42800000, v68
	v_mul_f32_e32 v160, 0x42800000, v76
	v_mov_b32_e32 v135, 0
	v_cvt_pk_fp8_f32 v135, v157, v160
	v_mul_f32_e32 v157, 0x42800000, v93
	v_mul_f32_e32 v160, 0x42800000, v101
	v_cvt_pk_fp8_f32 v164, v157, v160 op_sel:[0,0,1]
	v_mul_f32_e32 v157, 0x42800000, v92
	v_mul_f32_e32 v160, 0x42800000, v100
	v_cvt_pk_fp8_f32 v135, v157, v160 op_sel:[0,0,1]
	s_waitcnt vmcnt(23)
	v_mul_f32_e32 v157, 0x42800000, v94
	s_waitcnt vmcnt(22)
	v_mul_f32_e32 v161, 0x42800000, v102
	v_mov_b32_e32 v160, 0
	ds_write2_b32 v156, v162, v164 offset0:243 offset1:244
	v_cvt_pk_fp8_f32 v160, v157, v161
	v_mul_f32_e32 v157, 0x42800000, v95
	v_mul_f32_e32 v161, 0x42800000, v103
	v_mov_b32_e32 v164, 0
	v_cvt_pk_fp8_f32 v164, v157, v161
	s_waitcnt vmcnt(21)
	v_mul_f32_e32 v162, 0x42800000, v110
	s_waitcnt vmcnt(20)
	v_mul_f32_e32 v163, 0x42800000, v118
	v_mul_f32_e32 v157, 0x42800000, v111
	v_mul_f32_e32 v161, 0x42800000, v119
	v_cvt_pk_fp8_f32 v160, v162, v163 op_sel:[0,0,1]
	v_cvt_pk_fp8_f32 v164, v157, v161 op_sel:[0,0,1]
	v_mul_f32_e32 v157, 0x42800000, v96
	v_mul_f32_e32 v161, 0x42800000, v104
	v_mov_b32_e32 v162, 0
	v_cvt_pk_fp8_f32 v162, v157, v161
	v_mul_f32_e32 v157, 0x42800000, v97
	v_mul_f32_e32 v161, 0x42800000, v105
	v_mov_b32_e32 v166, 0
	v_cvt_pk_fp8_f32 v166, v157, v161
	v_mul_f32_e32 v163, 0x42800000, v112
	v_mul_f32_e32 v165, 0x42800000, v120
	v_mul_f32_e32 v157, 0x42800000, v113
	v_mul_f32_e32 v161, 0x42800000, v121
	v_cvt_pk_fp8_f32 v162, v163, v165 op_sel:[0,0,1]
	v_cvt_pk_fp8_f32 v166, v157, v161 op_sel:[0,0,1]
	s_waitcnt vmcnt(19)
	v_mul_f32_e32 v157, 0x42800000, v106
	s_waitcnt vmcnt(18)
	v_mul_f32_e32 v163, 0x42800000, v114
	v_mov_b32_e32 v161, 0
	v_cvt_pk_fp8_f32 v161, v157, v163
	v_mul_f32_e32 v157, 0x42800000, v107
	v_mul_f32_e32 v163, 0x42800000, v115
	v_mov_b32_e32 v168, 0
	v_cvt_pk_fp8_f32 v168, v157, v163
	s_waitcnt vmcnt(17)
	v_mul_f32_e32 v165, 0x42800000, v122
	s_waitcnt vmcnt(16)
	v_mul_f32_e32 v167, 0x42800000, v126
	v_mul_f32_e32 v157, 0x42800000, v123
	v_mul_f32_e32 v163, 0x42800000, v127
	v_cvt_pk_fp8_f32 v161, v165, v167 op_sel:[0,0,1]
	v_cvt_pk_fp8_f32 v168, v157, v163 op_sel:[0,0,1]
	v_mul_f32_e32 v157, 0x42800000, v108
	v_mul_f32_e32 v165, 0x42800000, v116
	v_mov_b32_e32 v163, 0
	v_cvt_pk_fp8_f32 v163, v157, v165
	v_mul_f32_e32 v157, 0x42800000, v109
	v_mul_f32_e32 v165, 0x42800000, v117
	v_mov_b32_e32 v170, 0
	v_cvt_pk_fp8_f32 v170, v157, v165
	v_mul_f32_e32 v167, 0x42800000, v124
	v_mul_f32_e32 v169, 0x42800000, v128
	v_cvt_pk_fp8_f32 v163, v167, v169 op_sel:[0,0,1]
	v_mul_f32_e32 v157, 0x42800000, v125
	v_mul_f32_e32 v165, 0x42800000, v129
	v_cvt_pk_fp8_f32 v170, v157, v165 op_sel:[0,0,1]
	ds_write_b128 v156, v[158:161] offset:192
	ds_write2_b32 v156, v164, v168 offset0:115 offset1:116
	ds_write2_b64 v156, v[134:135], v[162:163] offset0:89 offset1:90
	ds_write2_b32 v156, v166, v170 offset0:245 offset1:246
	v_cndmask_b32_e64 v134, 0, 1, s[4:5]
	v_cmp_ne_u32_e64 s[8:9], 1, v134
	s_andn2_b64 vcc, exec, s[4:5]
	s_mov_b64 s[4:5], -1
	s_cbranch_vccnz .LBB0_234
	s_add_i32 s1, s34, s31
	s_mov_b64 s[4:5], 0
.LBB0_234:
	s_andn2_b64 vcc, exec, s[4:5]
	s_lshl_b64 s[2:3], s[2:3], 22
	s_cbranch_vccz .Lcv2_b
	s_waitcnt vmcnt(0)
	s_branch .LBB0_229
.Lcv2_b:
	s_ashr_i32 s1, s33, 31
	s_lshr_b32 s1, s1, 24
	s_add_i32 s1, s33, s1
	s_ashr_i32 s4, s1, 8
	s_ashr_i32 s5, s4, 31
	s_lshl_b64 s[6:7], s[4:5], 24
	s_add_u32 s6, s14, s6
	s_addc_u32 s7, s15, s7
	s_and_b32 s1, s1, 0x7ff00
	s_sub_i32 s1, s33, s1
	s_lshr_b32 s1, s1, 3
	s_bfe_i32 s5, s1, 0x80000
	s_bfe_u32 s5, s5, 0x2000d
	s_add_i32 s5, s1, s5
	s_bfe_i32 s36, s5, 0x80000
	s_and_b32 s5, s5, 0xfc
	s_sub_i32 s1, s1, s5
	s_sext_i32_i8 s1, s1
	s_lshl_b32 s5, s1, 9
	s_add_i32 s1, s31, s34
	s_lshl_b32 s4, s4, 14
	s_sub_i32 s4, s1, s4
	s_and_b32 s34, s4, 0x100
	s_sext_i32_i16 s36, s36
	s_or_b32 s5, s5, s34
	v_or_b32_e32 v42, s5, v138
	s_lshl_b32 s5, s36, 6
	v_ashrrev_i32_e32 v43, 31, v42
	s_and_b32 s5, s5, 0xffffff00
	s_and_b32 s4, s4, 0xc0
	v_lshlrev_b64 v[42:43], 13, v[42:43]
	s_or_b32 s4, s5, s4
	v_lshl_add_u64 v[42:43], s[6:7], 0, v[42:43]
	s_ashr_i32 s5, s4, 31
	v_lshl_add_u64 v[42:43], s[4:5], 2, v[42:43]
	v_lshl_add_u64 v[122:123], v[196:197], 2, v[42:43]
	v_add_co_u32_e32 v46, vcc, s16, v122
	s_nop 1
	v_addc_co_u32_e32 v47, vcc, 0, v123, vcc
	v_add_co_u32_e32 v66, vcc, s17, v122
	global_load_dwordx4 v[42:45], v[122:123], off nt
	s_nop 0
	global_load_dwordx4 v[46:49], v[46:47], off nt
	v_addc_co_u32_e32 v67, vcc, 0, v123, vcc
	v_add_co_u32_e32 v68, vcc, s18, v122
	s_nop 1
	v_addc_co_u32_e32 v69, vcc, 0, v123, vcc
	global_load_dwordx4 v[70:73], v[66:67], off nt
	global_load_dwordx4 v[78:81], v[68:69], off nt
	v_add_co_u32_e32 v66, vcc, s19, v122
	s_nop 1
	v_addc_co_u32_e32 v67, vcc, 0, v123, vcc
	v_add_co_u32_e32 v74, vcc, s20, v122
	s_nop 1
	v_addc_co_u32_e32 v75, vcc, 0, v123, vcc
	v_add_co_u32_e32 v90, vcc, s21, v122
	global_load_dwordx4 v[66:69], v[66:67], off nt
	s_nop 0
	global_load_dwordx4 v[74:77], v[74:75], off nt
	v_addc_co_u32_e32 v91, vcc, 0, v123, vcc
	v_add_co_u32_e32 v94, vcc, s22, v122
	s_nop 1
	v_addc_co_u32_e32 v95, vcc, 0, v123, vcc
	global_load_dwordx4 v[90:93], v[90:91], off nt
	s_nop 0
	global_load_dwordx4 v[98:101], v[94:95], off nt
	v_add_co_u32_e32 v94, vcc, s23, v122
	s_nop 1
	v_addc_co_u32_e32 v95, vcc, 0, v123, vcc
	v_add_co_u32_e32 v102, vcc, s24, v122
	s_nop 1
	v_addc_co_u32_e32 v103, vcc, 0, v123, vcc
	v_add_co_u32_e32 v106, vcc, s25, v122
	global_load_dwordx4 v[94:97], v[94:95], off nt
	s_nop 0
	global_load_dwordx4 v[102:105], v[102:103], off nt
	v_addc_co_u32_e32 v107, vcc, 0, v123, vcc
	v_add_co_u32_e32 v108, vcc, s26, v122
	s_nop 1
	v_addc_co_u32_e32 v109, vcc, 0, v123, vcc
	global_load_dwordx4 v[110:113], v[106:107], off nt
	global_load_dwordx4 v[118:121], v[108:109], off nt
	v_add_co_u32_e32 v106, vcc, 0x18000, v122
	s_nop 1
	v_addc_co_u32_e32 v107, vcc, 0, v123, vcc
	v_add_co_u32_e32 v114, vcc, 0x1a000, v122
	s_nop 1
	v_addc_co_u32_e32 v115, vcc, 0, v123, vcc
	v_add_co_u32_e32 v124, vcc, 0x1c000, v122
	global_load_dwordx4 v[106:109], v[106:107], off nt
	s_nop 0
	global_load_dwordx4 v[114:117], v[114:115], off nt
	v_addc_co_u32_e32 v125, vcc, 0, v123, vcc
	v_add_co_u32_e32 v126, vcc, 0x1e000, v122
	s_nop 1
	v_addc_co_u32_e32 v127, vcc, 0, v123, vcc
	global_load_dwordx4 v[122:125], v[124:125], off nt
	s_nop 0
	global_load_dwordx4 v[126:129], v[126:127], off nt
	s_branch .LBB0_229
